# plus: GEMM K-loops without the adjacent s_setprio 0/1 pair between the two MFMA blocks of a phase
# baseline (speedup 1.0000x reference)
.LBB0_514:
	s_add_u32 s22, s82, s92
	s_addc_u32 s23, s83, s93
	s_add_u32 s24, s22, 0x100
	s_addc_u32 s25, s23, 0
	s_add_u32 s58, s3, s92
	s_addc_u32 s59, s2, s93
	s_add_i32 vcc_lo, 0, 0x10000
	s_cmpk_eq_i32 s92, 0xf00
	s_cselect_b64 s[26:27], -1, 0
	s_and_b64 s[22:23], s[26:27], exec
	s_cselect_b32 s25, s67, s25
	s_cselect_b32 s24, s75, s24
	s_cselect_b32 s23, s95, s59
	s_cselect_b32 s22, s29, s58
	s_add_i32 vcc_hi, 0, 0x14000
	v_add_u32_e32 v130, vcc_lo, v223
	v_add_u32_e32 v142, vcc_hi, v223
	ds_read_b128 v[146:149], v130
	ds_read_b128 v[150:153], v130 offset:1024
	ds_read_b128 v[154:157], v130 offset:2048
	ds_read_b128 v[158:161], v130 offset:3072
	ds_read_b128 v[130:133], v142
	ds_read_b128 v[134:137], v142 offset:1024
	ds_read_b128 v[138:141], v142 offset:2048
	ds_read_b128 v[142:145], v142 offset:3072
	v_lshl_add_u64 v[214:215], v[210:211], 0, s[92:93]
	s_add_i32 m0, s81, 0xc000
	s_waitcnt lgkmcnt(0)
	ds_read_b128 v[162:165], v224
	ds_read_b128 v[166:169], v224 offset:1024
	ds_read_b128 v[170:173], v224 offset:2048
	ds_read_b128 v[174:177], v224 offset:3072
	ds_read_b128 v[178:181], v224 offset:4096
	ds_read_b128 v[182:185], v224 offset:5120
	ds_read_b128 v[186:189], v224 offset:6144
	ds_read_b128 v[190:193], v224 offset:7168
	global_load_lds_dwordx4 v[214:215], off
	v_lshl_add_u64 v[214:215], v[212:213], 0, s[92:93]
	s_add_i32 m0, s81, 0xe000
	s_nop 0
	global_load_lds_dwordx4 v[214:215], off
	s_waitcnt vmcnt(8)
	s_waitcnt lgkmcnt(0)
	s_barrier
	s_setprio 1
	s_waitcnt lgkmcnt(0)
	v_mfma_f32_16x16x32_bf16 v[124:127], v[146:149], v[162:165], v[124:127]
	v_mfma_f32_16x16x32_bf16 v[120:123], v[154:157], v[162:165], v[120:123]
	v_mfma_f32_16x16x32_bf16 v[116:119], v[146:149], v[170:173], v[116:119]
	v_mfma_f32_16x16x32_bf16 v[108:111], v[154:157], v[170:173], v[108:111]
	v_mfma_f32_16x16x32_bf16 v[100:103], v[146:149], v[178:181], v[100:103]
	v_mfma_f32_16x16x32_bf16 v[92:95], v[154:157], v[178:181], v[92:95]
	v_mfma_f32_16x16x32_bf16 v[84:87], v[146:149], v[186:189], v[84:87]
	v_mfma_f32_16x16x32_bf16 v[76:79], v[154:157], v[186:189], v[76:79]
	v_mfma_f32_16x16x32_bf16 v[124:127], v[150:153], v[166:169], v[124:127]
	v_mfma_f32_16x16x32_bf16 v[120:123], v[158:161], v[166:169], v[120:123]
	v_mfma_f32_16x16x32_bf16 v[116:119], v[150:153], v[174:177], v[116:119]
	v_mfma_f32_16x16x32_bf16 v[108:111], v[158:161], v[174:177], v[108:111]
	v_mfma_f32_16x16x32_bf16 v[100:103], v[150:153], v[182:185], v[100:103]
	v_mfma_f32_16x16x32_bf16 v[92:95], v[158:161], v[182:185], v[92:95]
	v_mfma_f32_16x16x32_bf16 v[84:87], v[150:153], v[190:193], v[84:87]
	v_mfma_f32_16x16x32_bf16 v[76:79], v[158:161], v[190:193], v[76:79]
	v_mfma_f32_16x16x32_bf16 v[112:115], v[130:133], v[162:165], v[112:115]
	v_mfma_f32_16x16x32_bf16 v[104:107], v[138:141], v[162:165], v[104:107]
	v_mfma_f32_16x16x32_bf16 v[96:99], v[130:133], v[170:173], v[96:99]
	v_mfma_f32_16x16x32_bf16 v[88:91], v[138:141], v[170:173], v[88:91]
	v_mfma_f32_16x16x32_bf16 v[80:83], v[130:133], v[178:181], v[80:83]
	v_mfma_f32_16x16x32_bf16 v[72:75], v[138:141], v[178:181], v[72:75]
	v_mfma_f32_16x16x32_bf16 v[68:71], v[130:133], v[186:189], v[68:71]
	v_mfma_f32_16x16x32_bf16 v[64:67], v[138:141], v[186:189], v[64:67]
	v_mfma_f32_16x16x32_bf16 v[112:115], v[134:137], v[166:169], v[112:115]
	v_mfma_f32_16x16x32_bf16 v[104:107], v[142:145], v[166:169], v[104:107]
	v_mfma_f32_16x16x32_bf16 v[96:99], v[134:137], v[174:177], v[96:99]
	v_mfma_f32_16x16x32_bf16 v[88:91], v[142:145], v[174:177], v[88:91]
	v_mfma_f32_16x16x32_bf16 v[80:83], v[134:137], v[182:185], v[80:83]
	v_mfma_f32_16x16x32_bf16 v[72:75], v[142:145], v[182:185], v[72:75]
	v_mfma_f32_16x16x32_bf16 v[68:71], v[134:137], v[190:193], v[68:71]
	v_mfma_f32_16x16x32_bf16 v[64:67], v[142:145], v[190:193], v[64:67]
	s_setprio 0
	s_barrier
	s_add_i32 s58, vcc_lo, s28
	v_lshl_add_u64 v[214:215], s[22:23], 0, v[200:201]
	s_mov_b32 m0, s58
	ds_read_b128 v[186:189], v224 offset:16384
	ds_read_b128 v[190:193], v224 offset:17408
	ds_read_b128 v[178:181], v224 offset:18432
	ds_read_b128 v[182:185], v224 offset:19456
	ds_read_b128 v[170:173], v224 offset:20480
	ds_read_b128 v[174:177], v224 offset:21504
	ds_read_b128 v[162:165], v224 offset:22528
	ds_read_b128 v[166:169], v224 offset:23552
	global_load_lds_dwordx4 v[214:215], off
	s_add_i32 m0, s58, 0x2000
	s_add_u32 s58, s22, 0x80000
	v_lshl_add_u64 v[216:217], s[22:23], 0, v[204:205]
	s_addc_u32 s59, s23, 0
	s_add_i32 vcc_lo, vcc_hi, s28
	global_load_lds_dwordx4 v[216:217], off
	v_lshl_add_u64 v[218:219], s[58:59], 0, v[200:201]
	s_mov_b32 m0, vcc_lo
	v_lshl_add_u64 v[220:221], s[24:25], 0, v[202:203]
	global_load_lds_dwordx4 v[218:219], off
	v_lshl_add_u64 v[218:219], s[58:59], 0, v[204:205]
	s_add_i32 m0, vcc_lo, 0x2000
	v_cndmask_b32_e64 v194, 0, 1, s[96:97]
	global_load_lds_dwordx4 v[218:219], off
	v_lshl_add_u64 v[218:219], s[24:25], 0, v[198:199]
	s_mov_b32 m0, s81
	v_cmp_ne_u32_e64 s[58:59], 1, v194
	global_load_lds_dwordx4 v[218:219], off
	s_mov_b32 m0, s88
	s_andn2_b64 vcc, exec, s[96:97]
	global_load_lds_dwordx4 v[220:221], off
	s_waitcnt vmcnt(8)
	s_waitcnt lgkmcnt(0)
	s_barrier
	s_cbranch_vccnz .LBB0_516
	s_setprio 1
	s_waitcnt lgkmcnt(0)
	v_mfma_f32_16x16x32_bf16 v[60:63], v[146:149], v[186:189], v[60:63]
	v_mfma_f32_16x16x32_bf16 v[56:59], v[154:157], v[186:189], v[56:59]
	v_mfma_f32_16x16x32_bf16 v[44:47], v[146:149], v[178:181], v[44:47]
	v_mfma_f32_16x16x32_bf16 v[40:43], v[154:157], v[178:181], v[40:43]
	v_mfma_f32_16x16x32_bf16 v[28:31], v[146:149], v[170:173], v[28:31]
	v_mfma_f32_16x16x32_bf16 v[24:27], v[154:157], v[170:173], v[24:27]
	v_mfma_f32_16x16x32_bf16 v[12:15], v[146:149], v[162:165], v[12:15]
	v_mfma_f32_16x16x32_bf16 v[8:11], v[154:157], v[162:165], v[8:11]
	v_mfma_f32_16x16x32_bf16 v[60:63], v[150:153], v[190:193], v[60:63]
	v_mfma_f32_16x16x32_bf16 v[56:59], v[158:161], v[190:193], v[56:59]
	v_mfma_f32_16x16x32_bf16 v[44:47], v[150:153], v[182:185], v[44:47]
	v_mfma_f32_16x16x32_bf16 v[40:43], v[158:161], v[182:185], v[40:43]
	v_mfma_f32_16x16x32_bf16 v[28:31], v[150:153], v[174:177], v[28:31]
	v_mfma_f32_16x16x32_bf16 v[24:27], v[158:161], v[174:177], v[24:27]
	v_mfma_f32_16x16x32_bf16 v[12:15], v[150:153], v[166:169], v[12:15]
	v_mfma_f32_16x16x32_bf16 v[8:11], v[158:161], v[166:169], v[8:11]
	v_mfma_f32_16x16x32_bf16 v[52:55], v[130:133], v[186:189], v[52:55]
	v_mfma_f32_16x16x32_bf16 v[48:51], v[138:141], v[186:189], v[48:51]
	v_mfma_f32_16x16x32_bf16 v[36:39], v[130:133], v[178:181], v[36:39]
	v_mfma_f32_16x16x32_bf16 v[32:35], v[138:141], v[178:181], v[32:35]
	v_mfma_f32_16x16x32_bf16 v[20:23], v[130:133], v[170:173], v[20:23]
	v_mfma_f32_16x16x32_bf16 v[16:19], v[138:141], v[170:173], v[16:19]
	v_mfma_f32_16x16x32_bf16 v[4:7], v[130:133], v[162:165], v[4:7]
	v_mfma_f32_16x16x32_bf16 v[0:3], v[138:141], v[162:165], v[0:3]
	v_mfma_f32_16x16x32_bf16 v[52:55], v[134:137], v[190:193], v[52:55]
	v_mfma_f32_16x16x32_bf16 v[48:51], v[142:145], v[190:193], v[48:51]
	v_mfma_f32_16x16x32_bf16 v[36:39], v[134:137], v[182:185], v[36:39]
	v_mfma_f32_16x16x32_bf16 v[32:35], v[142:145], v[182:185], v[32:35]
	v_mfma_f32_16x16x32_bf16 v[20:23], v[134:137], v[174:177], v[20:23]
	v_mfma_f32_16x16x32_bf16 v[16:19], v[142:145], v[174:177], v[16:19]
	v_mfma_f32_16x16x32_bf16 v[4:7], v[134:137], v[166:169], v[4:7]
	v_mfma_f32_16x16x32_bf16 v[0:3], v[142:145], v[166:169], v[0:3]
	s_setprio 0
.LBB0_516:
	s_barrier
	s_add_i32 vcc_lo, 0, 0x18000
	s_add_i32 vcc_hi, 0, 0x1c000
	v_add_u32_e32 v130, vcc_lo, v223
	v_add_u32_e32 v142, vcc_hi, v223
	ds_read_b128 v[146:149], v130
	ds_read_b128 v[150:153], v130 offset:1024
	ds_read_b128 v[154:157], v130 offset:2048
	ds_read_b128 v[158:161], v130 offset:3072
	ds_read_b128 v[130:133], v142
	ds_read_b128 v[134:137], v142 offset:1024
	ds_read_b128 v[138:141], v142 offset:2048
	ds_read_b128 v[142:145], v142 offset:3072
	s_and_b64 s[26:27], s[26:27], exec
	s_cselect_b32 s27, s72, s86
	s_cselect_b32 s26, 0, s87
	s_add_u32 s24, s24, s27
	s_addc_u32 s25, s25, s26
	s_mov_b32 m0, s89
	v_lshl_add_u64 v[226:227], s[24:25], 0, v[198:199]
	s_waitcnt lgkmcnt(0)
	ds_read_b128 v[162:165], v224 offset:32768
	ds_read_b128 v[166:169], v224 offset:33792
	ds_read_b128 v[170:173], v224 offset:34816
	ds_read_b128 v[174:177], v224 offset:35840
	ds_read_b128 v[178:181], v224 offset:36864
	ds_read_b128 v[182:185], v224 offset:37888
	ds_read_b128 v[186:189], v224 offset:38912
	ds_read_b128 v[190:193], v224 offset:39936
	global_load_lds_dwordx4 v[226:227], off
	v_lshl_add_u64 v[226:227], s[24:25], 0, v[202:203]
	s_mov_b32 m0, s90
	s_nop 0
	global_load_lds_dwordx4 v[226:227], off
	s_waitcnt vmcnt(8)
	s_waitcnt lgkmcnt(0)
	s_barrier
	s_setprio 1
	s_waitcnt lgkmcnt(0)
	v_mfma_f32_16x16x32_bf16 v[124:127], v[146:149], v[162:165], v[124:127]
	v_mfma_f32_16x16x32_bf16 v[120:123], v[154:157], v[162:165], v[120:123]
	v_mfma_f32_16x16x32_bf16 v[116:119], v[146:149], v[170:173], v[116:119]
	v_mfma_f32_16x16x32_bf16 v[108:111], v[154:157], v[170:173], v[108:111]
	v_mfma_f32_16x16x32_bf16 v[100:103], v[146:149], v[178:181], v[100:103]
	v_mfma_f32_16x16x32_bf16 v[92:95], v[154:157], v[178:181], v[92:95]
	v_mfma_f32_16x16x32_bf16 v[84:87], v[146:149], v[186:189], v[84:87]
	v_mfma_f32_16x16x32_bf16 v[76:79], v[154:157], v[186:189], v[76:79]
	v_mfma_f32_16x16x32_bf16 v[124:127], v[150:153], v[166:169], v[124:127]
	v_mfma_f32_16x16x32_bf16 v[120:123], v[158:161], v[166:169], v[120:123]
	v_mfma_f32_16x16x32_bf16 v[116:119], v[150:153], v[174:177], v[116:119]
	v_mfma_f32_16x16x32_bf16 v[108:111], v[158:161], v[174:177], v[108:111]
	v_mfma_f32_16x16x32_bf16 v[100:103], v[150:153], v[182:185], v[100:103]
	v_mfma_f32_16x16x32_bf16 v[92:95], v[158:161], v[182:185], v[92:95]
	v_mfma_f32_16x16x32_bf16 v[84:87], v[150:153], v[190:193], v[84:87]
	v_mfma_f32_16x16x32_bf16 v[76:79], v[158:161], v[190:193], v[76:79]
	v_mfma_f32_16x16x32_bf16 v[112:115], v[130:133], v[162:165], v[112:115]
	v_mfma_f32_16x16x32_bf16 v[104:107], v[138:141], v[162:165], v[104:107]
	v_mfma_f32_16x16x32_bf16 v[96:99], v[130:133], v[170:173], v[96:99]
	v_mfma_f32_16x16x32_bf16 v[88:91], v[138:141], v[170:173], v[88:91]
	v_mfma_f32_16x16x32_bf16 v[80:83], v[130:133], v[178:181], v[80:83]
	v_mfma_f32_16x16x32_bf16 v[72:75], v[138:141], v[178:181], v[72:75]
	v_mfma_f32_16x16x32_bf16 v[68:71], v[130:133], v[186:189], v[68:71]
	v_mfma_f32_16x16x32_bf16 v[64:67], v[138:141], v[186:189], v[64:67]
	v_mfma_f32_16x16x32_bf16 v[112:115], v[134:137], v[166:169], v[112:115]
	v_mfma_f32_16x16x32_bf16 v[104:107], v[142:145], v[166:169], v[104:107]
	v_mfma_f32_16x16x32_bf16 v[96:99], v[134:137], v[174:177], v[96:99]
	v_mfma_f32_16x16x32_bf16 v[88:91], v[142:145], v[174:177], v[88:91]
	v_mfma_f32_16x16x32_bf16 v[80:83], v[134:137], v[182:185], v[80:83]
	v_mfma_f32_16x16x32_bf16 v[72:75], v[142:145], v[182:185], v[72:75]
	v_mfma_f32_16x16x32_bf16 v[68:71], v[134:137], v[190:193], v[68:71]
	v_mfma_f32_16x16x32_bf16 v[64:67], v[142:145], v[190:193], v[64:67]
	s_setprio 0
	s_barrier
	s_add_i32 s24, vcc_lo, s28
	v_lshl_add_u64 v[214:215], v[214:215], 0, s[42:43]
	s_mov_b32 m0, s24
	ds_read_b128 v[186:189], v224 offset:49152
	ds_read_b128 v[190:193], v224 offset:50176
	ds_read_b128 v[178:181], v224 offset:51200
	ds_read_b128 v[182:185], v224 offset:52224
	ds_read_b128 v[170:173], v224 offset:53248
	ds_read_b128 v[174:177], v224 offset:54272
	ds_read_b128 v[162:165], v224 offset:55296
	ds_read_b128 v[166:169], v224 offset:56320
	global_load_lds_dwordx4 v[214:215], off
	s_add_i32 m0, s24, 0x2000
	s_add_u32 s22, s22, 0x80080
	v_lshl_add_u64 v[214:215], v[216:217], 0, s[42:43]
	s_addc_u32 s23, s23, 0
	s_add_i32 s24, vcc_hi, s28
	global_load_lds_dwordx4 v[214:215], off
	v_lshl_add_u64 v[214:215], s[22:23], 0, v[200:201]
	s_mov_b32 m0, s24
	s_and_b64 vcc, exec, s[58:59]
	global_load_lds_dwordx4 v[214:215], off
	v_lshl_add_u64 v[214:215], s[22:23], 0, v[204:205]
	s_add_i32 m0, s24, 0x2000
	s_nop 0
	global_load_lds_dwordx4 v[214:215], off
	v_lshl_add_u64 v[214:215], v[218:219], 0, s[42:43]
	s_mov_b32 m0, s91
	s_nop 0
	global_load_lds_dwordx4 v[214:215], off
	v_lshl_add_u64 v[214:215], v[220:221], 0, s[42:43]
	s_mov_b32 m0, s94
	s_nop 0
	global_load_lds_dwordx4 v[214:215], off
	s_waitcnt vmcnt(8)
	s_waitcnt lgkmcnt(0)
	s_barrier
	s_cbranch_vccnz .LBB0_513
	s_setprio 1
	s_waitcnt lgkmcnt(0)
	v_mfma_f32_16x16x32_bf16 v[60:63], v[146:149], v[186:189], v[60:63]
	v_mfma_f32_16x16x32_bf16 v[56:59], v[154:157], v[186:189], v[56:59]
	v_mfma_f32_16x16x32_bf16 v[44:47], v[146:149], v[178:181], v[44:47]
	v_mfma_f32_16x16x32_bf16 v[40:43], v[154:157], v[178:181], v[40:43]
	v_mfma_f32_16x16x32_bf16 v[28:31], v[146:149], v[170:173], v[28:31]
	v_mfma_f32_16x16x32_bf16 v[24:27], v[154:157], v[170:173], v[24:27]
	v_mfma_f32_16x16x32_bf16 v[12:15], v[146:149], v[162:165], v[12:15]
	v_mfma_f32_16x16x32_bf16 v[8:11], v[154:157], v[162:165], v[8:11]
	v_mfma_f32_16x16x32_bf16 v[60:63], v[150:153], v[190:193], v[60:63]
	v_mfma_f32_16x16x32_bf16 v[56:59], v[158:161], v[190:193], v[56:59]
	v_mfma_f32_16x16x32_bf16 v[44:47], v[150:153], v[182:185], v[44:47]
	v_mfma_f32_16x16x32_bf16 v[40:43], v[158:161], v[182:185], v[40:43]
	v_mfma_f32_16x16x32_bf16 v[28:31], v[150:153], v[174:177], v[28:31]
	v_mfma_f32_16x16x32_bf16 v[24:27], v[158:161], v[174:177], v[24:27]
	v_mfma_f32_16x16x32_bf16 v[12:15], v[150:153], v[166:169], v[12:15]
	v_mfma_f32_16x16x32_bf16 v[8:11], v[158:161], v[166:169], v[8:11]
	v_mfma_f32_16x16x32_bf16 v[52:55], v[130:133], v[186:189], v[52:55]
	v_mfma_f32_16x16x32_bf16 v[48:51], v[138:141], v[186:189], v[48:51]
	v_mfma_f32_16x16x32_bf16 v[36:39], v[130:133], v[178:181], v[36:39]
	v_mfma_f32_16x16x32_bf16 v[32:35], v[138:141], v[178:181], v[32:35]
	v_mfma_f32_16x16x32_bf16 v[20:23], v[130:133], v[170:173], v[20:23]
	v_mfma_f32_16x16x32_bf16 v[16:19], v[138:141], v[170:173], v[16:19]
	v_mfma_f32_16x16x32_bf16 v[4:7], v[130:133], v[162:165], v[4:7]
	v_mfma_f32_16x16x32_bf16 v[0:3], v[138:141], v[162:165], v[0:3]
	v_mfma_f32_16x16x32_bf16 v[52:55], v[134:137], v[190:193], v[52:55]
	v_mfma_f32_16x16x32_bf16 v[48:51], v[142:145], v[190:193], v[48:51]
	v_mfma_f32_16x16x32_bf16 v[36:39], v[134:137], v[182:185], v[36:39]
	v_mfma_f32_16x16x32_bf16 v[32:35], v[142:145], v[182:185], v[32:35]
	v_mfma_f32_16x16x32_bf16 v[20:23], v[134:137], v[174:177], v[20:23]
	v_mfma_f32_16x16x32_bf16 v[16:19], v[142:145], v[174:177], v[16:19]
	v_mfma_f32_16x16x32_bf16 v[4:7], v[134:137], v[166:169], v[4:7]
	v_mfma_f32_16x16x32_bf16 v[0:3], v[142:145], v[166:169], v[0:3]
	s_setprio 0
	s_branch .LBB0_513

.LBB0_725:
	s_add_u32 s2, s64, 0xfffe0080
	s_addc_u32 s3, s65, -1
	s_add_i32 s29, 0, 0x10000
	s_cmp_eq_u32 s66, 4
	s_cselect_b32 s25, s61, s3
	s_cselect_b32 s24, s60, s2
	v_add_u32_e32 v145, s29, v143
	s_cselect_b32 s23, s63, s17
	s_cselect_b32 s22, s62, s15
	s_add_i32 s30, 0, 0x14000
	ds_read_b128 v[146:149], v145
	ds_read_b128 v[150:153], v145 offset:1024
	ds_read_b128 v[154:157], v145 offset:2048
	ds_read_b128 v[158:161], v145 offset:3072
	v_add_u32_e32 v145, s30, v143
	ds_read_b128 v[162:165], v145
	ds_read_b128 v[166:169], v145 offset:1024
	ds_read_b128 v[170:173], v145 offset:2048
	ds_read_b128 v[174:177], v145 offset:3072
	v_lshl_add_u64 v[214:215], s[64:65], 0, v[138:139]
	s_add_i32 m0, s53, 0xc000
	ds_read_b128 v[178:181], v144
	ds_read_b128 v[182:185], v144 offset:1024
	ds_read_b128 v[186:189], v144 offset:2048
	ds_read_b128 v[190:193], v144 offset:3072
	ds_read_b128 v[198:201], v144 offset:4096
	ds_read_b128 v[202:205], v144 offset:5120
	ds_read_b128 v[206:209], v144 offset:6144
	ds_read_b128 v[210:213], v144 offset:7168
	global_load_lds_dwordx4 v[214:215], off
	v_lshl_add_u64 v[214:215], s[64:65], 0, v[140:141]
	s_add_i32 m0, s53, 0xe000
	s_nop 0
	global_load_lds_dwordx4 v[214:215], off
	s_waitcnt vmcnt(8)
	s_waitcnt lgkmcnt(0)
	s_barrier
	s_setprio 1
	s_waitcnt lgkmcnt(0)
	v_mfma_f32_16x16x32_bf16 v[124:127], v[146:149], v[178:181], v[124:127]
	v_mfma_f32_16x16x32_bf16 v[120:123], v[154:157], v[178:181], v[120:123]
	v_mfma_f32_16x16x32_bf16 v[116:119], v[146:149], v[186:189], v[116:119]
	v_mfma_f32_16x16x32_bf16 v[108:111], v[154:157], v[186:189], v[108:111]
	v_mfma_f32_16x16x32_bf16 v[100:103], v[146:149], v[198:201], v[100:103]
	v_mfma_f32_16x16x32_bf16 v[92:95], v[154:157], v[198:201], v[92:95]
	v_mfma_f32_16x16x32_bf16 v[84:87], v[146:149], v[206:209], v[84:87]
	v_mfma_f32_16x16x32_bf16 v[76:79], v[154:157], v[206:209], v[76:79]
	v_mfma_f32_16x16x32_bf16 v[124:127], v[150:153], v[182:185], v[124:127]
	v_mfma_f32_16x16x32_bf16 v[120:123], v[158:161], v[182:185], v[120:123]
	v_mfma_f32_16x16x32_bf16 v[116:119], v[150:153], v[190:193], v[116:119]
	v_mfma_f32_16x16x32_bf16 v[108:111], v[158:161], v[190:193], v[108:111]
	v_mfma_f32_16x16x32_bf16 v[100:103], v[150:153], v[202:205], v[100:103]
	v_mfma_f32_16x16x32_bf16 v[92:95], v[158:161], v[202:205], v[92:95]
	v_mfma_f32_16x16x32_bf16 v[84:87], v[150:153], v[210:213], v[84:87]
	v_mfma_f32_16x16x32_bf16 v[76:79], v[158:161], v[210:213], v[76:79]
	v_mfma_f32_16x16x32_bf16 v[112:115], v[162:165], v[178:181], v[112:115]
	v_mfma_f32_16x16x32_bf16 v[104:107], v[170:173], v[178:181], v[104:107]
	v_mfma_f32_16x16x32_bf16 v[96:99], v[162:165], v[186:189], v[96:99]
	v_mfma_f32_16x16x32_bf16 v[88:91], v[170:173], v[186:189], v[88:91]
	v_mfma_f32_16x16x32_bf16 v[80:83], v[162:165], v[198:201], v[80:83]
	v_mfma_f32_16x16x32_bf16 v[72:75], v[170:173], v[198:201], v[72:75]
	v_mfma_f32_16x16x32_bf16 v[68:71], v[162:165], v[206:209], v[68:71]
	v_mfma_f32_16x16x32_bf16 v[64:67], v[170:173], v[206:209], v[64:67]
	v_mfma_f32_16x16x32_bf16 v[112:115], v[166:169], v[182:185], v[112:115]
	v_mfma_f32_16x16x32_bf16 v[104:107], v[174:177], v[182:185], v[104:107]
	v_mfma_f32_16x16x32_bf16 v[96:99], v[166:169], v[190:193], v[96:99]
	v_mfma_f32_16x16x32_bf16 v[88:91], v[174:177], v[190:193], v[88:91]
	v_mfma_f32_16x16x32_bf16 v[80:83], v[166:169], v[202:205], v[80:83]
	v_mfma_f32_16x16x32_bf16 v[72:75], v[174:177], v[202:205], v[72:75]
	v_mfma_f32_16x16x32_bf16 v[68:71], v[166:169], v[210:213], v[68:71]
	v_mfma_f32_16x16x32_bf16 v[64:67], v[174:177], v[210:213], v[64:67]
	s_setprio 0
	s_barrier
	s_add_i32 s2, s29, s39
	v_lshl_add_u64 v[214:215], s[22:23], 0, v[134:135]
	s_mov_b32 m0, s2
	ds_read_b128 v[178:181], v144 offset:16384
	ds_read_b128 v[182:185], v144 offset:17408
	ds_read_b128 v[186:189], v144 offset:18432
	ds_read_b128 v[190:193], v144 offset:19456
	ds_read_b128 v[198:201], v144 offset:20480
	ds_read_b128 v[202:205], v144 offset:21504
	ds_read_b128 v[206:209], v144 offset:22528
	ds_read_b128 v[210:213], v144 offset:23552
	global_load_lds_dwordx4 v[214:215], off
	s_add_i32 m0, s2, 0x2000
	s_add_u32 s2, s22, 0x20000
	v_lshl_add_u64 v[216:217], s[22:23], 0, v[130:131]
	s_addc_u32 s3, s23, 0
	s_add_i32 s29, s30, s39
	global_load_lds_dwordx4 v[216:217], off
	v_lshl_add_u64 v[218:219], s[2:3], 0, v[134:135]
	s_mov_b32 m0, s29
	v_lshl_add_u64 v[220:221], s[24:25], 0, v[132:133]
	global_load_lds_dwordx4 v[218:219], off
	v_lshl_add_u64 v[218:219], s[2:3], 0, v[130:131]
	s_add_i32 m0, s29, 0x2000
	s_nop 0
	global_load_lds_dwordx4 v[218:219], off
	v_lshl_add_u64 v[218:219], s[24:25], 0, v[136:137]
	s_mov_b32 m0, s53
	s_nop 0
	global_load_lds_dwordx4 v[218:219], off
	s_mov_b32 m0, s68
	s_nop 0
	global_load_lds_dwordx4 v[220:221], off
	s_waitcnt vmcnt(8)
	s_waitcnt lgkmcnt(0)
	s_barrier
	s_setprio 1
	s_waitcnt lgkmcnt(0)
	v_mfma_f32_16x16x32_bf16 v[60:63], v[146:149], v[178:181], v[60:63]
	v_mfma_f32_16x16x32_bf16 v[56:59], v[154:157], v[178:181], v[56:59]
	v_mfma_f32_16x16x32_bf16 v[52:55], v[146:149], v[186:189], v[52:55]
	v_mfma_f32_16x16x32_bf16 v[44:47], v[154:157], v[186:189], v[44:47]
	v_mfma_f32_16x16x32_bf16 v[36:39], v[146:149], v[198:201], v[36:39]
	v_mfma_f32_16x16x32_bf16 v[28:31], v[154:157], v[198:201], v[28:31]
	v_mfma_f32_16x16x32_bf16 v[20:23], v[146:149], v[206:209], v[20:23]
	v_mfma_f32_16x16x32_bf16 v[12:15], v[154:157], v[206:209], v[12:15]
	v_mfma_f32_16x16x32_bf16 v[60:63], v[150:153], v[182:185], v[60:63]
	v_mfma_f32_16x16x32_bf16 v[56:59], v[158:161], v[182:185], v[56:59]
	v_mfma_f32_16x16x32_bf16 v[52:55], v[150:153], v[190:193], v[52:55]
	v_mfma_f32_16x16x32_bf16 v[44:47], v[158:161], v[190:193], v[44:47]
	v_mfma_f32_16x16x32_bf16 v[36:39], v[150:153], v[202:205], v[36:39]
	v_mfma_f32_16x16x32_bf16 v[28:31], v[158:161], v[202:205], v[28:31]
	v_mfma_f32_16x16x32_bf16 v[20:23], v[150:153], v[210:213], v[20:23]
	v_mfma_f32_16x16x32_bf16 v[12:15], v[158:161], v[210:213], v[12:15]
	v_mfma_f32_16x16x32_bf16 v[48:51], v[162:165], v[178:181], v[48:51]
	v_mfma_f32_16x16x32_bf16 v[40:43], v[170:173], v[178:181], v[40:43]
	v_mfma_f32_16x16x32_bf16 v[32:35], v[162:165], v[186:189], v[32:35]
	v_mfma_f32_16x16x32_bf16 v[24:27], v[170:173], v[186:189], v[24:27]
	v_mfma_f32_16x16x32_bf16 v[16:19], v[162:165], v[198:201], v[16:19]
	v_mfma_f32_16x16x32_bf16 v[8:11], v[170:173], v[198:201], v[8:11]
	v_mfma_f32_16x16x32_bf16 v[4:7], v[162:165], v[206:209], v[4:7]
	v_mfma_f32_16x16x32_bf16 v[0:3], v[170:173], v[206:209], v[0:3]
	v_mfma_f32_16x16x32_bf16 v[48:51], v[166:169], v[182:185], v[48:51]
	v_mfma_f32_16x16x32_bf16 v[40:43], v[174:177], v[182:185], v[40:43]
	v_mfma_f32_16x16x32_bf16 v[32:35], v[166:169], v[190:193], v[32:35]
	v_mfma_f32_16x16x32_bf16 v[24:27], v[174:177], v[190:193], v[24:27]
	v_mfma_f32_16x16x32_bf16 v[16:19], v[166:169], v[202:205], v[16:19]
	v_mfma_f32_16x16x32_bf16 v[8:11], v[174:177], v[202:205], v[8:11]
	v_mfma_f32_16x16x32_bf16 v[4:7], v[166:169], v[210:213], v[4:7]
	v_mfma_f32_16x16x32_bf16 v[0:3], v[174:177], v[210:213], v[0:3]
	s_setprio 0
	s_barrier
	s_add_i32 s29, 0, 0x18000
	v_add_u32_e32 v145, s29, v143
	s_add_i32 s30, 0, 0x1c000
	ds_read_b128 v[146:149], v145
	ds_read_b128 v[150:153], v145 offset:1024
	ds_read_b128 v[154:157], v145 offset:2048
	ds_read_b128 v[158:161], v145 offset:3072
	v_add_u32_e32 v145, s30, v143
	ds_read_b128 v[162:165], v145
	ds_read_b128 v[166:169], v145 offset:1024
	ds_read_b128 v[170:173], v145 offset:2048
	ds_read_b128 v[174:177], v145 offset:3072
	s_add_u32 s2, s24, 0x20000
	s_addc_u32 s3, s25, 0
	s_mov_b32 m0, s69
	v_lshl_add_u64 v[222:223], s[2:3], 0, v[136:137]
	ds_read_b128 v[178:181], v144 offset:32768
	ds_read_b128 v[182:185], v144 offset:33792
	ds_read_b128 v[186:189], v144 offset:34816
	ds_read_b128 v[190:193], v144 offset:35840
	ds_read_b128 v[198:201], v144 offset:36864
	ds_read_b128 v[202:205], v144 offset:37888
	ds_read_b128 v[206:209], v144 offset:38912
	ds_read_b128 v[210:213], v144 offset:39936
	global_load_lds_dwordx4 v[222:223], off
	v_lshl_add_u64 v[222:223], s[2:3], 0, v[132:133]
	s_mov_b32 m0, s70
	s_nop 0
	global_load_lds_dwordx4 v[222:223], off
	s_waitcnt vmcnt(8)
	s_waitcnt lgkmcnt(0)
	s_barrier
	s_setprio 1
	s_waitcnt lgkmcnt(0)
	v_mfma_f32_16x16x32_bf16 v[124:127], v[146:149], v[178:181], v[124:127]
	v_mfma_f32_16x16x32_bf16 v[120:123], v[154:157], v[178:181], v[120:123]
	v_mfma_f32_16x16x32_bf16 v[116:119], v[146:149], v[186:189], v[116:119]
	v_mfma_f32_16x16x32_bf16 v[108:111], v[154:157], v[186:189], v[108:111]
	v_mfma_f32_16x16x32_bf16 v[100:103], v[146:149], v[198:201], v[100:103]
	v_mfma_f32_16x16x32_bf16 v[92:95], v[154:157], v[198:201], v[92:95]
	v_mfma_f32_16x16x32_bf16 v[84:87], v[146:149], v[206:209], v[84:87]
	v_mfma_f32_16x16x32_bf16 v[76:79], v[154:157], v[206:209], v[76:79]
	v_mfma_f32_16x16x32_bf16 v[124:127], v[150:153], v[182:185], v[124:127]
	v_mfma_f32_16x16x32_bf16 v[120:123], v[158:161], v[182:185], v[120:123]
	v_mfma_f32_16x16x32_bf16 v[116:119], v[150:153], v[190:193], v[116:119]
	v_mfma_f32_16x16x32_bf16 v[108:111], v[158:161], v[190:193], v[108:111]
	v_mfma_f32_16x16x32_bf16 v[100:103], v[150:153], v[202:205], v[100:103]
	v_mfma_f32_16x16x32_bf16 v[92:95], v[158:161], v[202:205], v[92:95]
	v_mfma_f32_16x16x32_bf16 v[84:87], v[150:153], v[210:213], v[84:87]
	v_mfma_f32_16x16x32_bf16 v[76:79], v[158:161], v[210:213], v[76:79]
	v_mfma_f32_16x16x32_bf16 v[112:115], v[162:165], v[178:181], v[112:115]
	v_mfma_f32_16x16x32_bf16 v[104:107], v[170:173], v[178:181], v[104:107]
	v_mfma_f32_16x16x32_bf16 v[96:99], v[162:165], v[186:189], v[96:99]
	v_mfma_f32_16x16x32_bf16 v[88:91], v[170:173], v[186:189], v[88:91]
	v_mfma_f32_16x16x32_bf16 v[80:83], v[162:165], v[198:201], v[80:83]
	v_mfma_f32_16x16x32_bf16 v[72:75], v[170:173], v[198:201], v[72:75]
	v_mfma_f32_16x16x32_bf16 v[68:71], v[162:165], v[206:209], v[68:71]
	v_mfma_f32_16x16x32_bf16 v[64:67], v[170:173], v[206:209], v[64:67]
	v_mfma_f32_16x16x32_bf16 v[112:115], v[166:169], v[182:185], v[112:115]
	v_mfma_f32_16x16x32_bf16 v[104:107], v[174:177], v[182:185], v[104:107]
	v_mfma_f32_16x16x32_bf16 v[96:99], v[166:169], v[190:193], v[96:99]
	v_mfma_f32_16x16x32_bf16 v[88:91], v[174:177], v[190:193], v[88:91]
	v_mfma_f32_16x16x32_bf16 v[80:83], v[166:169], v[202:205], v[80:83]
	v_mfma_f32_16x16x32_bf16 v[72:75], v[174:177], v[202:205], v[72:75]
	v_mfma_f32_16x16x32_bf16 v[68:71], v[166:169], v[210:213], v[68:71]
	v_mfma_f32_16x16x32_bf16 v[64:67], v[174:177], v[210:213], v[64:67]
	s_setprio 0
	s_barrier
	s_add_i32 s2, s29, s39
	v_lshl_add_u64 v[214:215], v[214:215], 0, s[42:43]
	s_mov_b32 m0, s2
	ds_read_b128 v[178:181], v144 offset:49152
	ds_read_b128 v[182:185], v144 offset:50176
	ds_read_b128 v[186:189], v144 offset:51200
	ds_read_b128 v[190:193], v144 offset:52224
	ds_read_b128 v[198:201], v144 offset:53248
	ds_read_b128 v[202:205], v144 offset:54272
	ds_read_b128 v[206:209], v144 offset:55296
	ds_read_b128 v[210:213], v144 offset:56320
	global_load_lds_dwordx4 v[214:215], off
	s_add_i32 m0, s2, 0x2000
	s_add_u32 s2, s22, 0x20080
	v_lshl_add_u64 v[214:215], v[216:217], 0, s[42:43]
	s_addc_u32 s3, s23, 0
	s_add_i32 s22, s30, s39
	global_load_lds_dwordx4 v[214:215], off
	v_lshl_add_u64 v[214:215], s[2:3], 0, v[134:135]
	s_mov_b32 m0, s22
	s_nop 0
	global_load_lds_dwordx4 v[214:215], off
	v_lshl_add_u64 v[214:215], s[2:3], 0, v[130:131]
	s_add_i32 m0, s22, 0x2000
	s_nop 0
	global_load_lds_dwordx4 v[214:215], off
	v_lshl_add_u64 v[214:215], v[218:219], 0, s[42:43]
	s_mov_b32 m0, s71
	s_nop 0
	global_load_lds_dwordx4 v[214:215], off
	v_lshl_add_u64 v[214:215], v[220:221], 0, s[42:43]
	s_mov_b32 m0, s74
	s_nop 0
	global_load_lds_dwordx4 v[214:215], off
	s_waitcnt vmcnt(8)
	s_waitcnt lgkmcnt(0)
	s_barrier
	s_setprio 1
	s_waitcnt lgkmcnt(0)
	v_mfma_f32_16x16x32_bf16 v[60:63], v[146:149], v[178:181], v[60:63]
	v_mfma_f32_16x16x32_bf16 v[56:59], v[154:157], v[178:181], v[56:59]
	v_mfma_f32_16x16x32_bf16 v[52:55], v[146:149], v[186:189], v[52:55]
	v_mfma_f32_16x16x32_bf16 v[44:47], v[154:157], v[186:189], v[44:47]
	v_mfma_f32_16x16x32_bf16 v[36:39], v[146:149], v[198:201], v[36:39]
	v_mfma_f32_16x16x32_bf16 v[28:31], v[154:157], v[198:201], v[28:31]
	v_mfma_f32_16x16x32_bf16 v[20:23], v[146:149], v[206:209], v[20:23]
	v_mfma_f32_16x16x32_bf16 v[12:15], v[154:157], v[206:209], v[12:15]
	v_mfma_f32_16x16x32_bf16 v[60:63], v[150:153], v[182:185], v[60:63]
	v_mfma_f32_16x16x32_bf16 v[56:59], v[158:161], v[182:185], v[56:59]
	v_mfma_f32_16x16x32_bf16 v[52:55], v[150:153], v[190:193], v[52:55]
	v_mfma_f32_16x16x32_bf16 v[44:47], v[158:161], v[190:193], v[44:47]
	v_mfma_f32_16x16x32_bf16 v[36:39], v[150:153], v[202:205], v[36:39]
	v_mfma_f32_16x16x32_bf16 v[28:31], v[158:161], v[202:205], v[28:31]
	v_mfma_f32_16x16x32_bf16 v[20:23], v[150:153], v[210:213], v[20:23]
	v_mfma_f32_16x16x32_bf16 v[12:15], v[158:161], v[210:213], v[12:15]
	v_mfma_f32_16x16x32_bf16 v[48:51], v[162:165], v[178:181], v[48:51]
	v_mfma_f32_16x16x32_bf16 v[40:43], v[170:173], v[178:181], v[40:43]
	v_mfma_f32_16x16x32_bf16 v[32:35], v[162:165], v[186:189], v[32:35]
	v_mfma_f32_16x16x32_bf16 v[24:27], v[170:173], v[186:189], v[24:27]
	v_mfma_f32_16x16x32_bf16 v[16:19], v[162:165], v[198:201], v[16:19]
	v_mfma_f32_16x16x32_bf16 v[8:11], v[170:173], v[198:201], v[8:11]
	v_mfma_f32_16x16x32_bf16 v[4:7], v[162:165], v[206:209], v[4:7]
	v_mfma_f32_16x16x32_bf16 v[0:3], v[170:173], v[206:209], v[0:3]
	v_mfma_f32_16x16x32_bf16 v[48:51], v[166:169], v[182:185], v[48:51]
	v_mfma_f32_16x16x32_bf16 v[40:43], v[174:177], v[182:185], v[40:43]
	v_mfma_f32_16x16x32_bf16 v[32:35], v[166:169], v[190:193], v[32:35]
	v_mfma_f32_16x16x32_bf16 v[24:27], v[174:177], v[190:193], v[24:27]
	v_mfma_f32_16x16x32_bf16 v[16:19], v[166:169], v[202:205], v[16:19]
	v_mfma_f32_16x16x32_bf16 v[8:11], v[174:177], v[202:205], v[8:11]
	v_mfma_f32_16x16x32_bf16 v[4:7], v[166:169], v[210:213], v[4:7]
	v_mfma_f32_16x16x32_bf16 v[0:3], v[174:177], v[210:213], v[0:3]
	s_setprio 0
	s_barrier
	s_add_i32 s66, s66, 2
	s_add_u32 s64, s64, 0x100
	s_addc_u32 s65, s65, 0
	s_add_u32 s15, s15, 0x100
	s_addc_u32 s17, s17, 0
	s_cmp_gt_u32 s66, 5
	s_cbranch_scc0 .LBB0_725
	s_and_b64 vcc, exec, s[10:11]
	s_cbranch_vccz .LBB0_728
	s_barrier

.LBB0_969:
	s_add_u32 s24, s18, s92
	s_addc_u32 s25, s19, s93
	s_add_u32 s60, s24, 0x100
	s_addc_u32 s61, s25, 0
	s_add_u32 s81, s2, s92
	s_addc_u32 s84, s29, s93
	s_add_i32 vcc_lo, 0, 0x10000
	s_cmpk_eq_i32 s92, 0xf00
	s_cselect_b64 s[26:27], -1, 0
	s_and_b64 s[24:25], s[26:27], exec
	s_cselect_b32 s25, s15, s61
	s_cselect_b32 s24, s17, s60
	s_waitcnt lgkmcnt(0)
	v_add_u32_e32 v104, vcc_lo, v234
	s_cselect_b32 s85, s67, s84
	s_cselect_b32 s84, s3, s81
	s_add_i32 s81, 0, 0x14000
	ds_read_b128 v[162:165], v104
	ds_read_b128 v[166:169], v104 offset:1024
	ds_read_b128 v[170:173], v104 offset:2048
	ds_read_b128 v[174:177], v104 offset:3072
	v_add_u32_e32 v104, s81, v234
	ds_read_b128 v[146:149], v104
	ds_read_b128 v[150:153], v104 offset:1024
	ds_read_b128 v[154:157], v104 offset:2048
	ds_read_b128 v[158:161], v104 offset:3072
	v_lshl_add_u64 v[104:105], v[208:209], 0, s[92:93]
	s_add_i32 m0, s53, 0xc000
	ds_read_b128 v[178:181], v236
	ds_read_b128 v[182:185], v236 offset:1024
	ds_read_b128 v[186:189], v236 offset:2048
	ds_read_b128 v[190:193], v236 offset:3072
	ds_read_b128 v[210:213], v236 offset:4096
	ds_read_b128 v[214:217], v236 offset:5120
	ds_read_b128 v[218:221], v236 offset:6144
	ds_read_b128 v[222:225], v236 offset:7168
	global_load_lds_dwordx4 v[104:105], off
	v_lshl_add_u64 v[104:105], v[206:207], 0, s[92:93]
	s_add_i32 m0, s53, 0xe000
	s_nop 0
	global_load_lds_dwordx4 v[104:105], off
	s_waitcnt vmcnt(8)
	s_waitcnt lgkmcnt(0)
	s_barrier
	s_setprio 1
	s_waitcnt lgkmcnt(0)
	v_mfma_f32_16x16x32_bf16 v[104:107], v[162:165], v[178:181], v[142:145]
	v_mfma_f32_16x16x32_bf16 v[108:111], v[170:173], v[178:181], v[138:141]
	v_mfma_f32_16x16x32_bf16 v[116:119], v[162:165], v[186:189], v[120:123]
	v_mfma_f32_16x16x32_bf16 v[112:115], v[170:173], v[186:189], v[112:115]
	v_mfma_f32_16x16x32_bf16 v[92:95], v[162:165], v[210:213], v[92:95]
	v_mfma_f32_16x16x32_bf16 v[88:91], v[170:173], v[210:213], v[88:91]
	v_mfma_f32_16x16x32_bf16 v[76:79], v[162:165], v[218:221], v[76:79]
	v_mfma_f32_16x16x32_bf16 v[72:75], v[170:173], v[218:221], v[72:75]
	v_mfma_f32_16x16x32_bf16 v[104:107], v[166:169], v[182:185], v[104:107]
	v_mfma_f32_16x16x32_bf16 v[108:111], v[174:177], v[182:185], v[108:111]
	v_mfma_f32_16x16x32_bf16 v[116:119], v[166:169], v[190:193], v[116:119]
	v_mfma_f32_16x16x32_bf16 v[112:115], v[174:177], v[190:193], v[112:115]
	v_mfma_f32_16x16x32_bf16 v[92:95], v[166:169], v[214:217], v[92:95]
	v_mfma_f32_16x16x32_bf16 v[88:91], v[174:177], v[214:217], v[88:91]
	v_mfma_f32_16x16x32_bf16 v[76:79], v[166:169], v[222:225], v[76:79]
	v_mfma_f32_16x16x32_bf16 v[72:75], v[174:177], v[222:225], v[72:75]
	v_mfma_f32_16x16x32_bf16 v[120:123], v[146:149], v[178:181], v[134:137]
	v_mfma_f32_16x16x32_bf16 v[130:133], v[150:153], v[182:185], v[120:123]
	v_mfma_f32_16x16x32_bf16 v[120:123], v[154:157], v[178:181], v[124:127]
	v_mfma_f32_16x16x32_bf16 v[100:103], v[146:149], v[186:189], v[100:103]
	v_mfma_f32_16x16x32_bf16 v[96:99], v[154:157], v[186:189], v[96:99]
	v_mfma_f32_16x16x32_bf16 v[84:87], v[146:149], v[210:213], v[84:87]
	v_mfma_f32_16x16x32_bf16 v[80:83], v[154:157], v[210:213], v[80:83]
	v_mfma_f32_16x16x32_bf16 v[68:71], v[146:149], v[218:221], v[68:71]
	v_mfma_f32_16x16x32_bf16 v[64:67], v[154:157], v[218:221], v[64:67]
	v_mfma_f32_16x16x32_bf16 v[124:127], v[158:161], v[182:185], v[120:123]
	v_mfma_f32_16x16x32_bf16 v[100:103], v[150:153], v[190:193], v[100:103]
	v_mfma_f32_16x16x32_bf16 v[96:99], v[158:161], v[190:193], v[96:99]
	v_mfma_f32_16x16x32_bf16 v[84:87], v[150:153], v[214:217], v[84:87]
	v_mfma_f32_16x16x32_bf16 v[80:83], v[158:161], v[214:217], v[80:83]
	v_mfma_f32_16x16x32_bf16 v[68:71], v[150:153], v[222:225], v[68:71]
	v_mfma_f32_16x16x32_bf16 v[64:67], v[158:161], v[222:225], v[64:67]
	s_setprio 0
	s_barrier
	s_add_i32 s60, vcc_lo, s39
	v_lshl_add_u64 v[210:211], s[84:85], 0, v[198:199]
	s_mov_b32 m0, s60
	ds_read_b128 v[186:189], v236 offset:16384
	ds_read_b128 v[190:193], v236 offset:17408
	ds_read_b128 v[178:181], v236 offset:18432
	ds_read_b128 v[182:185], v236 offset:19456
	ds_read_b128 v[138:141], v236 offset:20480
	ds_read_b128 v[142:145], v236 offset:21504
	ds_read_b128 v[120:123], v236 offset:22528
	ds_read_b128 v[134:137], v236 offset:23552
	global_load_lds_dwordx4 v[210:211], off
	s_add_i32 m0, s60, 0x2000
	s_add_u32 s60, s84, 0x80000
	v_lshl_add_u64 v[212:213], s[84:85], 0, v[200:201]
	s_addc_u32 s61, s85, 0
	s_add_i32 s81, s81, s39
	global_load_lds_dwordx4 v[212:213], off
	v_lshl_add_u64 v[214:215], s[60:61], 0, v[198:199]
	s_mov_b32 m0, s81
	v_lshl_add_u64 v[216:217], s[24:25], 0, v[200:201]
	global_load_lds_dwordx4 v[214:215], off
	v_lshl_add_u64 v[214:215], s[60:61], 0, v[200:201]
	s_add_i32 m0, s81, 0x2000
	v_cndmask_b32_e64 v128, 0, 1, s[96:97]
	global_load_lds_dwordx4 v[214:215], off
	v_lshl_add_u64 v[214:215], s[24:25], 0, v[198:199]
	s_mov_b32 m0, s53
	v_cmp_ne_u32_e64 s[60:61], 1, v128
	global_load_lds_dwordx4 v[214:215], off
	s_mov_b32 m0, s88
	s_andn2_b64 vcc, exec, s[96:97]
	global_load_lds_dwordx4 v[216:217], off
	s_waitcnt vmcnt(8)
	s_waitcnt lgkmcnt(0)
	s_barrier
	s_cbranch_vccnz .LBB0_971
	s_setprio 1
	s_waitcnt lgkmcnt(0)
	v_mfma_f32_16x16x32_bf16 v[60:63], v[162:165], v[186:189], v[60:63]
	v_mfma_f32_16x16x32_bf16 v[56:59], v[170:173], v[186:189], v[56:59]
	v_mfma_f32_16x16x32_bf16 v[44:47], v[162:165], v[178:181], v[44:47]
	v_mfma_f32_16x16x32_bf16 v[40:43], v[170:173], v[178:181], v[40:43]
	v_mfma_f32_16x16x32_bf16 v[28:31], v[162:165], v[138:141], v[28:31]
	v_mfma_f32_16x16x32_bf16 v[24:27], v[170:173], v[138:141], v[24:27]
	v_mfma_f32_16x16x32_bf16 v[12:15], v[162:165], v[120:123], v[12:15]
	v_mfma_f32_16x16x32_bf16 v[8:11], v[170:173], v[120:123], v[8:11]
	v_mfma_f32_16x16x32_bf16 v[60:63], v[166:169], v[190:193], v[60:63]
	v_mfma_f32_16x16x32_bf16 v[56:59], v[174:177], v[190:193], v[56:59]
	v_mfma_f32_16x16x32_bf16 v[44:47], v[166:169], v[182:185], v[44:47]
	v_mfma_f32_16x16x32_bf16 v[40:43], v[174:177], v[182:185], v[40:43]
	v_mfma_f32_16x16x32_bf16 v[28:31], v[166:169], v[142:145], v[28:31]
	v_mfma_f32_16x16x32_bf16 v[24:27], v[174:177], v[142:145], v[24:27]
	v_mfma_f32_16x16x32_bf16 v[12:15], v[166:169], v[134:137], v[12:15]
	v_mfma_f32_16x16x32_bf16 v[8:11], v[174:177], v[134:137], v[8:11]
	v_mfma_f32_16x16x32_bf16 v[52:55], v[146:149], v[186:189], v[52:55]
	v_mfma_f32_16x16x32_bf16 v[48:51], v[154:157], v[186:189], v[48:51]
	v_mfma_f32_16x16x32_bf16 v[36:39], v[146:149], v[178:181], v[36:39]
	v_mfma_f32_16x16x32_bf16 v[32:35], v[154:157], v[178:181], v[32:35]
	v_mfma_f32_16x16x32_bf16 v[20:23], v[146:149], v[138:141], v[20:23]
	v_mfma_f32_16x16x32_bf16 v[16:19], v[154:157], v[138:141], v[16:19]
	v_mfma_f32_16x16x32_bf16 v[4:7], v[146:149], v[120:123], v[4:7]
	v_mfma_f32_16x16x32_bf16 v[0:3], v[154:157], v[120:123], v[0:3]
	v_mfma_f32_16x16x32_bf16 v[52:55], v[150:153], v[190:193], v[52:55]
	v_mfma_f32_16x16x32_bf16 v[48:51], v[158:161], v[190:193], v[48:51]
	v_mfma_f32_16x16x32_bf16 v[36:39], v[150:153], v[182:185], v[36:39]
	v_mfma_f32_16x16x32_bf16 v[32:35], v[158:161], v[182:185], v[32:35]
	v_mfma_f32_16x16x32_bf16 v[20:23], v[150:153], v[142:145], v[20:23]
	v_mfma_f32_16x16x32_bf16 v[16:19], v[158:161], v[142:145], v[16:19]
	v_mfma_f32_16x16x32_bf16 v[4:7], v[150:153], v[134:137], v[4:7]
	v_mfma_f32_16x16x32_bf16 v[0:3], v[158:161], v[134:137], v[0:3]
	s_setprio 0
.LBB0_971:
	s_barrier
	s_add_i32 s81, 0, 0x18000
	s_waitcnt lgkmcnt(0)
	v_add_u32_e32 v120, s81, v234
	s_add_i32 vcc_lo, 0, 0x1c000
	ds_read_b128 v[162:165], v120
	ds_read_b128 v[166:169], v120 offset:1024
	ds_read_b128 v[170:173], v120 offset:2048
	ds_read_b128 v[174:177], v120 offset:3072
	v_add_u32_e32 v120, vcc_lo, v234
	ds_read_b128 v[146:149], v120
	ds_read_b128 v[150:153], v120 offset:1024
	ds_read_b128 v[154:157], v120 offset:2048
	ds_read_b128 v[158:161], v120 offset:3072
	s_and_b64 s[26:27], s[26:27], exec
	s_cselect_b32 s27, s72, s20
	s_cselect_b32 s26, 0, s21
	s_add_u32 s24, s24, s27
	s_addc_u32 s25, s25, s26
	s_mov_b32 m0, s89
	v_lshl_add_u64 v[120:121], s[24:25], 0, v[198:199]
	ds_read_b128 v[178:181], v236 offset:32768
	ds_read_b128 v[182:185], v236 offset:33792
	ds_read_b128 v[186:189], v236 offset:34816
	ds_read_b128 v[190:193], v236 offset:35840
	ds_read_b128 v[218:221], v236 offset:36864
	ds_read_b128 v[222:225], v236 offset:37888
	ds_read_b128 v[226:229], v236 offset:38912
	ds_read_b128 v[238:241], v236 offset:39936
	global_load_lds_dwordx4 v[120:121], off
	v_lshl_add_u64 v[120:121], s[24:25], 0, v[200:201]
	s_mov_b32 m0, s90
	s_nop 0
	global_load_lds_dwordx4 v[120:121], off
	s_waitcnt vmcnt(8)
	s_waitcnt lgkmcnt(0)
	s_barrier
	s_setprio 1
	s_waitcnt lgkmcnt(0)
	v_mfma_f32_16x16x32_bf16 v[104:107], v[162:165], v[178:181], v[104:107]
	v_mfma_f32_16x16x32_bf16 v[142:145], v[166:169], v[182:185], v[104:107]
	v_mfma_f32_16x16x32_bf16 v[104:107], v[170:173], v[178:181], v[108:111]
	v_mfma_f32_16x16x32_bf16 v[138:141], v[174:177], v[182:185], v[104:107]
	v_mfma_f32_16x16x32_bf16 v[104:107], v[162:165], v[186:189], v[116:119]
	v_mfma_f32_16x16x32_bf16 v[120:123], v[166:169], v[190:193], v[104:107]
	v_mfma_f32_16x16x32_bf16 v[104:107], v[170:173], v[186:189], v[112:115]
	v_mfma_f32_16x16x32_bf16 v[92:95], v[162:165], v[218:221], v[92:95]
	v_mfma_f32_16x16x32_bf16 v[88:91], v[170:173], v[218:221], v[88:91]
	v_mfma_f32_16x16x32_bf16 v[76:79], v[162:165], v[226:229], v[76:79]
	v_mfma_f32_16x16x32_bf16 v[72:75], v[170:173], v[226:229], v[72:75]
	v_mfma_f32_16x16x32_bf16 v[112:115], v[174:177], v[190:193], v[104:107]
	v_mfma_f32_16x16x32_bf16 v[92:95], v[166:169], v[222:225], v[92:95]
	v_mfma_f32_16x16x32_bf16 v[88:91], v[174:177], v[222:225], v[88:91]
	v_mfma_f32_16x16x32_bf16 v[76:79], v[166:169], v[238:241], v[76:79]
	v_mfma_f32_16x16x32_bf16 v[72:75], v[174:177], v[238:241], v[72:75]
	v_mfma_f32_16x16x32_bf16 v[104:107], v[146:149], v[178:181], v[130:133]
	v_mfma_f32_16x16x32_bf16 v[134:137], v[150:153], v[182:185], v[104:107]
	v_mfma_f32_16x16x32_bf16 v[104:107], v[154:157], v[178:181], v[124:127]
	v_mfma_f32_16x16x32_bf16 v[100:103], v[146:149], v[186:189], v[100:103]
	v_mfma_f32_16x16x32_bf16 v[96:99], v[154:157], v[186:189], v[96:99]
	v_mfma_f32_16x16x32_bf16 v[84:87], v[146:149], v[218:221], v[84:87]
	v_mfma_f32_16x16x32_bf16 v[80:83], v[154:157], v[218:221], v[80:83]
	v_mfma_f32_16x16x32_bf16 v[68:71], v[146:149], v[226:229], v[68:71]
	v_mfma_f32_16x16x32_bf16 v[64:67], v[154:157], v[226:229], v[64:67]
	v_mfma_f32_16x16x32_bf16 v[124:127], v[158:161], v[182:185], v[104:107]
	v_mfma_f32_16x16x32_bf16 v[100:103], v[150:153], v[190:193], v[100:103]
	v_mfma_f32_16x16x32_bf16 v[96:99], v[158:161], v[190:193], v[96:99]
	v_mfma_f32_16x16x32_bf16 v[84:87], v[150:153], v[222:225], v[84:87]
	v_mfma_f32_16x16x32_bf16 v[80:83], v[158:161], v[222:225], v[80:83]
	v_mfma_f32_16x16x32_bf16 v[68:71], v[150:153], v[238:241], v[68:71]
	v_mfma_f32_16x16x32_bf16 v[64:67], v[158:161], v[238:241], v[64:67]
	s_setprio 0
	s_barrier
	s_add_i32 s24, s81, s39
	v_lshl_add_u64 v[210:211], v[210:211], 0, s[42:43]
	s_mov_b32 m0, s24
	ds_read_b128 v[186:189], v236 offset:49152
	ds_read_b128 v[190:193], v236 offset:50176
	ds_read_b128 v[178:181], v236 offset:51200
	ds_read_b128 v[182:185], v236 offset:52224
	ds_read_b128 v[116:119], v236 offset:53248
	ds_read_b128 v[130:133], v236 offset:54272
	ds_read_b128 v[104:107], v236 offset:55296
	ds_read_b128 v[108:111], v236 offset:56320
	global_load_lds_dwordx4 v[210:211], off
	s_add_i32 m0, s24, 0x2000
	s_add_u32 s24, s84, 0x80080
	v_lshl_add_u64 v[210:211], v[212:213], 0, s[42:43]
	s_addc_u32 s25, s85, 0
	s_add_i32 s26, vcc_lo, s39
	global_load_lds_dwordx4 v[210:211], off
	v_lshl_add_u64 v[210:211], s[24:25], 0, v[198:199]
	s_mov_b32 m0, s26
	s_and_b64 vcc, exec, s[60:61]
	global_load_lds_dwordx4 v[210:211], off
	v_lshl_add_u64 v[210:211], s[24:25], 0, v[200:201]
	s_add_i32 m0, s26, 0x2000
	s_nop 0
	global_load_lds_dwordx4 v[210:211], off
	v_lshl_add_u64 v[210:211], v[214:215], 0, s[42:43]
	s_mov_b32 m0, s94
	s_nop 0
	global_load_lds_dwordx4 v[210:211], off
	v_lshl_add_u64 v[210:211], v[216:217], 0, s[42:43]
	s_mov_b32 m0, s33
	s_nop 0
	global_load_lds_dwordx4 v[210:211], off
	s_waitcnt vmcnt(8)
	s_waitcnt lgkmcnt(0)
	s_barrier
	s_cbranch_vccnz .LBB0_968
	s_setprio 1
	s_waitcnt lgkmcnt(0)
	v_mfma_f32_16x16x32_bf16 v[60:63], v[162:165], v[186:189], v[60:63]
	v_mfma_f32_16x16x32_bf16 v[56:59], v[170:173], v[186:189], v[56:59]
	v_mfma_f32_16x16x32_bf16 v[44:47], v[162:165], v[178:181], v[44:47]
	v_mfma_f32_16x16x32_bf16 v[40:43], v[170:173], v[178:181], v[40:43]
	v_mfma_f32_16x16x32_bf16 v[28:31], v[162:165], v[116:119], v[28:31]
	v_mfma_f32_16x16x32_bf16 v[24:27], v[170:173], v[116:119], v[24:27]
	v_mfma_f32_16x16x32_bf16 v[12:15], v[162:165], v[104:107], v[12:15]
	v_mfma_f32_16x16x32_bf16 v[8:11], v[170:173], v[104:107], v[8:11]
	v_mfma_f32_16x16x32_bf16 v[60:63], v[166:169], v[190:193], v[60:63]
	v_mfma_f32_16x16x32_bf16 v[56:59], v[174:177], v[190:193], v[56:59]
	v_mfma_f32_16x16x32_bf16 v[44:47], v[166:169], v[182:185], v[44:47]
	v_mfma_f32_16x16x32_bf16 v[40:43], v[174:177], v[182:185], v[40:43]
	v_mfma_f32_16x16x32_bf16 v[28:31], v[166:169], v[130:133], v[28:31]
	v_mfma_f32_16x16x32_bf16 v[24:27], v[174:177], v[130:133], v[24:27]
	v_mfma_f32_16x16x32_bf16 v[12:15], v[166:169], v[108:111], v[12:15]
	v_mfma_f32_16x16x32_bf16 v[8:11], v[174:177], v[108:111], v[8:11]
	v_mfma_f32_16x16x32_bf16 v[52:55], v[146:149], v[186:189], v[52:55]
	v_mfma_f32_16x16x32_bf16 v[48:51], v[154:157], v[186:189], v[48:51]
	v_mfma_f32_16x16x32_bf16 v[36:39], v[146:149], v[178:181], v[36:39]
	v_mfma_f32_16x16x32_bf16 v[32:35], v[154:157], v[178:181], v[32:35]
	v_mfma_f32_16x16x32_bf16 v[20:23], v[146:149], v[116:119], v[20:23]
	v_mfma_f32_16x16x32_bf16 v[16:19], v[154:157], v[116:119], v[16:19]
	v_mfma_f32_16x16x32_bf16 v[4:7], v[146:149], v[104:107], v[4:7]
	v_mfma_f32_16x16x32_bf16 v[0:3], v[154:157], v[104:107], v[0:3]
	v_mfma_f32_16x16x32_bf16 v[52:55], v[150:153], v[190:193], v[52:55]
	v_mfma_f32_16x16x32_bf16 v[48:51], v[158:161], v[190:193], v[48:51]
	v_mfma_f32_16x16x32_bf16 v[36:39], v[150:153], v[182:185], v[36:39]
	v_mfma_f32_16x16x32_bf16 v[32:35], v[158:161], v[182:185], v[32:35]
	v_mfma_f32_16x16x32_bf16 v[20:23], v[150:153], v[130:133], v[20:23]
	v_mfma_f32_16x16x32_bf16 v[16:19], v[158:161], v[130:133], v[16:19]
	v_mfma_f32_16x16x32_bf16 v[4:7], v[150:153], v[108:111], v[4:7]
	v_mfma_f32_16x16x32_bf16 v[0:3], v[158:161], v[108:111], v[0:3]
	s_setprio 0
	s_branch .LBB0_968

.LBB0_1400:
	s_add_u32 s2, s64, s74
	s_addc_u32 s3, s65, s75
	s_add_u32 s22, s2, 0x28c00100
	s_addc_u32 s23, s3, 0
	s_cmpk_eq_i32 s74, 0xf00
	s_cselect_b64 s[60:61], -1, 0
	s_and_b64 s[2:3], s[60:61], exec
	s_cselect_b32 s23, s9, s23
	s_cselect_b32 s22, s8, s22
	v_add_u32_e32 v128, s26, v242
	s_add_i32 s2, 0, 0x14000
	v_lshl_add_u64 v[146:147], v[220:221], 0, s[74:75]
	ds_read_b128 v[130:133], v128
	ds_read_b128 v[134:137], v128 offset:1024
	ds_read_b128 v[138:141], v128 offset:2048
	ds_read_b128 v[142:145], v128 offset:3072
	v_add_u32_e32 v128, s2, v242
	v_cndmask_b32_e64 v223, v147, v207, s[60:61]
	v_cndmask_b32_e64 v222, v146, v206, s[60:61]
	ds_read_b128 v[146:149], v128
	ds_read_b128 v[150:153], v128 offset:1024
	ds_read_b128 v[154:157], v128 offset:2048
	ds_read_b128 v[158:161], v128 offset:3072
	v_lshl_add_u64 v[194:195], v[218:219], 0, s[74:75]
	s_add_i32 m0, s36, 0xc000
	s_waitcnt lgkmcnt(0)
	ds_read_b128 v[162:165], v209
	ds_read_b128 v[166:169], v209 offset:1024
	ds_read_b128 v[170:173], v209 offset:2048
	ds_read_b128 v[174:177], v209 offset:3072
	ds_read_b128 v[178:181], v209 offset:4096
	ds_read_b128 v[182:185], v209 offset:5120
	ds_read_b128 v[186:189], v209 offset:6144
	ds_read_b128 v[190:193], v209 offset:7168
	global_load_lds_dwordx4 v[194:195], off
	v_lshl_add_u64 v[194:195], v[216:217], 0, s[74:75]
	s_add_i32 m0, s36, 0xe000
	s_nop 0
	global_load_lds_dwordx4 v[194:195], off
	s_waitcnt vmcnt(8)
	s_waitcnt lgkmcnt(0)
	s_barrier
	s_setprio 1
	s_waitcnt lgkmcnt(0)
	v_mfma_f32_16x16x32_bf16 v[124:127], v[130:133], v[162:165], v[124:127]
	v_mfma_f32_16x16x32_bf16 v[120:123], v[138:141], v[162:165], v[120:123]
	v_mfma_f32_16x16x32_bf16 v[108:111], v[130:133], v[170:173], v[108:111]
	v_mfma_f32_16x16x32_bf16 v[104:107], v[138:141], v[170:173], v[104:107]
	v_mfma_f32_16x16x32_bf16 v[92:95], v[130:133], v[178:181], v[92:95]
	v_mfma_f32_16x16x32_bf16 v[88:91], v[138:141], v[178:181], v[88:91]
	v_mfma_f32_16x16x32_bf16 v[76:79], v[130:133], v[186:189], v[76:79]
	v_mfma_f32_16x16x32_bf16 v[72:75], v[138:141], v[186:189], v[72:75]
	v_mfma_f32_16x16x32_bf16 v[124:127], v[134:137], v[166:169], v[124:127]
	v_mfma_f32_16x16x32_bf16 v[120:123], v[142:145], v[166:169], v[120:123]
	v_mfma_f32_16x16x32_bf16 v[108:111], v[134:137], v[174:177], v[108:111]
	v_mfma_f32_16x16x32_bf16 v[104:107], v[142:145], v[174:177], v[104:107]
	v_mfma_f32_16x16x32_bf16 v[92:95], v[134:137], v[182:185], v[92:95]
	v_mfma_f32_16x16x32_bf16 v[88:91], v[142:145], v[182:185], v[88:91]
	v_mfma_f32_16x16x32_bf16 v[76:79], v[134:137], v[190:193], v[76:79]
	v_mfma_f32_16x16x32_bf16 v[72:75], v[142:145], v[190:193], v[72:75]
	v_mfma_f32_16x16x32_bf16 v[116:119], v[146:149], v[162:165], v[116:119]
	v_mfma_f32_16x16x32_bf16 v[112:115], v[154:157], v[162:165], v[112:115]
	v_mfma_f32_16x16x32_bf16 v[100:103], v[146:149], v[170:173], v[100:103]
	v_mfma_f32_16x16x32_bf16 v[96:99], v[154:157], v[170:173], v[96:99]
	v_mfma_f32_16x16x32_bf16 v[84:87], v[146:149], v[178:181], v[84:87]
	v_mfma_f32_16x16x32_bf16 v[80:83], v[154:157], v[178:181], v[80:83]
	v_mfma_f32_16x16x32_bf16 v[68:71], v[146:149], v[186:189], v[68:71]
	v_mfma_f32_16x16x32_bf16 v[64:67], v[154:157], v[186:189], v[64:67]
	v_mfma_f32_16x16x32_bf16 v[116:119], v[150:153], v[166:169], v[116:119]
	v_mfma_f32_16x16x32_bf16 v[112:115], v[158:161], v[166:169], v[112:115]
	v_mfma_f32_16x16x32_bf16 v[100:103], v[150:153], v[174:177], v[100:103]
	v_mfma_f32_16x16x32_bf16 v[96:99], v[158:161], v[174:177], v[96:99]
	v_mfma_f32_16x16x32_bf16 v[84:87], v[150:153], v[182:185], v[84:87]
	v_mfma_f32_16x16x32_bf16 v[80:83], v[158:161], v[182:185], v[80:83]
	v_mfma_f32_16x16x32_bf16 v[68:71], v[150:153], v[190:193], v[68:71]
	v_mfma_f32_16x16x32_bf16 v[64:67], v[158:161], v[190:193], v[64:67]
	s_setprio 0
	s_barrier
	s_add_i32 s3, s26, s33
	v_lshl_add_u64 v[224:225], v[222:223], 0, v[198:199]
	s_mov_b32 m0, s3
	ds_read_b128 v[186:189], v209 offset:16384
	ds_read_b128 v[190:193], v209 offset:17408
	ds_read_b128 v[178:181], v209 offset:18432
	ds_read_b128 v[182:185], v209 offset:19456
	ds_read_b128 v[170:173], v209 offset:20480
	ds_read_b128 v[174:177], v209 offset:21504
	ds_read_b128 v[162:165], v209 offset:22528
	ds_read_b128 v[166:169], v209 offset:23552
	global_load_lds_dwordx4 v[224:225], off
	v_lshl_add_u64 v[226:227], v[222:223], 0, v[200:201]
	s_add_i32 m0, s3, 0x2000
	v_lshl_add_u64 v[194:195], v[222:223], 0, s[40:41]
	s_add_i32 s2, s2, s33
	global_load_lds_dwordx4 v[226:227], off
	v_lshl_add_u64 v[196:197], v[194:195], 0, v[198:199]
	s_mov_b32 m0, s2
	v_lshl_add_u64 v[194:195], v[194:195], 0, v[200:201]
	global_load_lds_dwordx4 v[196:197], off
	s_add_i32 m0, s2, 0x2000
	v_cndmask_b32_e64 v128, v208, v211, s[60:61]
	global_load_lds_dwordx4 v[194:195], off
	s_mov_b32 m0, s36
	v_cndmask_b32_e64 v228, v210, v243, s[60:61]
	global_load_lds_dwordx4 v128, s[22:23]
	s_mov_b32 m0, s37
	v_cndmask_b32_e64 v194, 0, 1, s[20:21]
	global_load_lds_dwordx4 v228, s[22:23]
	s_waitcnt vmcnt(8)
	s_waitcnt lgkmcnt(0)
	v_cmp_ne_u32_e64 s[62:63], 1, v194
	s_andn2_b64 vcc, exec, s[20:21]
	s_barrier
	s_cbranch_vccnz .LBB0_1402
	s_setprio 1
	s_waitcnt lgkmcnt(0)
	v_mfma_f32_16x16x32_bf16 v[60:63], v[130:133], v[186:189], v[60:63]
	v_mfma_f32_16x16x32_bf16 v[56:59], v[138:141], v[186:189], v[56:59]
	v_mfma_f32_16x16x32_bf16 v[44:47], v[130:133], v[178:181], v[44:47]
	v_mfma_f32_16x16x32_bf16 v[40:43], v[138:141], v[178:181], v[40:43]
	v_mfma_f32_16x16x32_bf16 v[28:31], v[130:133], v[170:173], v[28:31]
	v_mfma_f32_16x16x32_bf16 v[24:27], v[138:141], v[170:173], v[24:27]
	v_mfma_f32_16x16x32_bf16 v[12:15], v[130:133], v[162:165], v[12:15]
	v_mfma_f32_16x16x32_bf16 v[8:11], v[138:141], v[162:165], v[8:11]
	v_mfma_f32_16x16x32_bf16 v[60:63], v[134:137], v[190:193], v[60:63]
	v_mfma_f32_16x16x32_bf16 v[56:59], v[142:145], v[190:193], v[56:59]
	v_mfma_f32_16x16x32_bf16 v[44:47], v[134:137], v[182:185], v[44:47]
	v_mfma_f32_16x16x32_bf16 v[40:43], v[142:145], v[182:185], v[40:43]
	v_mfma_f32_16x16x32_bf16 v[28:31], v[134:137], v[174:177], v[28:31]
	v_mfma_f32_16x16x32_bf16 v[24:27], v[142:145], v[174:177], v[24:27]
	v_mfma_f32_16x16x32_bf16 v[12:15], v[134:137], v[166:169], v[12:15]
	v_mfma_f32_16x16x32_bf16 v[8:11], v[142:145], v[166:169], v[8:11]
	v_mfma_f32_16x16x32_bf16 v[52:55], v[146:149], v[186:189], v[52:55]
	v_mfma_f32_16x16x32_bf16 v[48:51], v[154:157], v[186:189], v[48:51]
	v_mfma_f32_16x16x32_bf16 v[36:39], v[146:149], v[178:181], v[36:39]
	v_mfma_f32_16x16x32_bf16 v[32:35], v[154:157], v[178:181], v[32:35]
	v_mfma_f32_16x16x32_bf16 v[20:23], v[146:149], v[170:173], v[20:23]
	v_mfma_f32_16x16x32_bf16 v[16:19], v[154:157], v[170:173], v[16:19]
	v_mfma_f32_16x16x32_bf16 v[4:7], v[146:149], v[162:165], v[4:7]
	v_mfma_f32_16x16x32_bf16 v[0:3], v[154:157], v[162:165], v[0:3]
	v_mfma_f32_16x16x32_bf16 v[52:55], v[150:153], v[190:193], v[52:55]
	v_mfma_f32_16x16x32_bf16 v[48:51], v[158:161], v[190:193], v[48:51]
	v_mfma_f32_16x16x32_bf16 v[36:39], v[150:153], v[182:185], v[36:39]
	v_mfma_f32_16x16x32_bf16 v[32:35], v[158:161], v[182:185], v[32:35]
	v_mfma_f32_16x16x32_bf16 v[20:23], v[150:153], v[174:177], v[20:23]
	v_mfma_f32_16x16x32_bf16 v[16:19], v[158:161], v[174:177], v[16:19]
	v_mfma_f32_16x16x32_bf16 v[4:7], v[150:153], v[166:169], v[4:7]
	v_mfma_f32_16x16x32_bf16 v[0:3], v[158:161], v[166:169], v[0:3]
	s_setprio 0
.LBB0_1402:
	v_mov_b32_e32 v229, v129
	v_lshl_add_u64 v[194:195], s[22:23], 0, v[128:129]
	v_lshl_add_u64 v[196:197], s[22:23], 0, v[228:229]
	s_barrier
	s_add_i32 s2, 0, 0x18000
	v_add_u32_e32 v128, s2, v242
	s_add_i32 s3, 0, 0x1c000
	ds_read_b128 v[146:149], v128
	ds_read_b128 v[150:153], v128 offset:1024
	ds_read_b128 v[154:157], v128 offset:2048
	ds_read_b128 v[158:161], v128 offset:3072
	v_add_u32_e32 v128, s3, v242
	ds_read_b128 v[130:133], v128
	ds_read_b128 v[134:137], v128 offset:1024
	ds_read_b128 v[138:141], v128 offset:2048
	ds_read_b128 v[142:145], v128 offset:3072
	s_mov_b32 m0, s38
	v_cndmask_b32_e64 v128, v212, v244, s[60:61]
	s_waitcnt lgkmcnt(0)
	ds_read_b128 v[162:165], v209 offset:32768
	ds_read_b128 v[166:169], v209 offset:33792
	ds_read_b128 v[170:173], v209 offset:34816
	ds_read_b128 v[174:177], v209 offset:35840
	ds_read_b128 v[178:181], v209 offset:36864
	ds_read_b128 v[182:185], v209 offset:37888
	ds_read_b128 v[186:189], v209 offset:38912
	ds_read_b128 v[190:193], v209 offset:39936
	global_load_lds_dwordx4 v128, s[22:23]
	v_cndmask_b32_e64 v128, v214, v245, s[60:61]
	s_mov_b32 m0, s39
	s_nop 0
	global_load_lds_dwordx4 v128, s[22:23]
	s_waitcnt vmcnt(8)
	s_waitcnt lgkmcnt(0)
	s_barrier
	s_setprio 1
	s_waitcnt lgkmcnt(0)
	v_mfma_f32_16x16x32_bf16 v[124:127], v[146:149], v[162:165], v[124:127]
	v_mfma_f32_16x16x32_bf16 v[120:123], v[154:157], v[162:165], v[120:123]
	v_mfma_f32_16x16x32_bf16 v[108:111], v[146:149], v[170:173], v[108:111]
	v_mfma_f32_16x16x32_bf16 v[104:107], v[154:157], v[170:173], v[104:107]
	v_mfma_f32_16x16x32_bf16 v[92:95], v[146:149], v[178:181], v[92:95]
	v_mfma_f32_16x16x32_bf16 v[88:91], v[154:157], v[178:181], v[88:91]
	v_mfma_f32_16x16x32_bf16 v[76:79], v[146:149], v[186:189], v[76:79]
	v_mfma_f32_16x16x32_bf16 v[72:75], v[154:157], v[186:189], v[72:75]
	v_mfma_f32_16x16x32_bf16 v[124:127], v[150:153], v[166:169], v[124:127]
	v_mfma_f32_16x16x32_bf16 v[120:123], v[158:161], v[166:169], v[120:123]
	v_mfma_f32_16x16x32_bf16 v[108:111], v[150:153], v[174:177], v[108:111]
	v_mfma_f32_16x16x32_bf16 v[104:107], v[158:161], v[174:177], v[104:107]
	v_mfma_f32_16x16x32_bf16 v[92:95], v[150:153], v[182:185], v[92:95]
	v_mfma_f32_16x16x32_bf16 v[88:91], v[158:161], v[182:185], v[88:91]
	v_mfma_f32_16x16x32_bf16 v[76:79], v[150:153], v[190:193], v[76:79]
	v_mfma_f32_16x16x32_bf16 v[72:75], v[158:161], v[190:193], v[72:75]
	v_mfma_f32_16x16x32_bf16 v[116:119], v[130:133], v[162:165], v[116:119]
	v_mfma_f32_16x16x32_bf16 v[112:115], v[138:141], v[162:165], v[112:115]
	v_mfma_f32_16x16x32_bf16 v[100:103], v[130:133], v[170:173], v[100:103]
	v_mfma_f32_16x16x32_bf16 v[96:99], v[138:141], v[170:173], v[96:99]
	v_mfma_f32_16x16x32_bf16 v[84:87], v[130:133], v[178:181], v[84:87]
	v_mfma_f32_16x16x32_bf16 v[80:83], v[138:141], v[178:181], v[80:83]
	v_mfma_f32_16x16x32_bf16 v[68:71], v[130:133], v[186:189], v[68:71]
	v_mfma_f32_16x16x32_bf16 v[64:67], v[138:141], v[186:189], v[64:67]
	v_mfma_f32_16x16x32_bf16 v[116:119], v[134:137], v[166:169], v[116:119]
	v_mfma_f32_16x16x32_bf16 v[112:115], v[142:145], v[166:169], v[112:115]
	v_mfma_f32_16x16x32_bf16 v[100:103], v[134:137], v[174:177], v[100:103]
	v_mfma_f32_16x16x32_bf16 v[96:99], v[142:145], v[174:177], v[96:99]
	v_mfma_f32_16x16x32_bf16 v[84:87], v[134:137], v[182:185], v[84:87]
	v_mfma_f32_16x16x32_bf16 v[80:83], v[142:145], v[182:185], v[80:83]
	v_mfma_f32_16x16x32_bf16 v[68:71], v[134:137], v[190:193], v[68:71]
	v_mfma_f32_16x16x32_bf16 v[64:67], v[142:145], v[190:193], v[64:67]
	s_setprio 0
	s_barrier
	s_add_i32 s2, s2, s33
	v_lshl_add_u64 v[224:225], v[224:225], 0, s[42:43]
	s_mov_b32 m0, s2
	ds_read_b128 v[186:189], v209 offset:49152
	ds_read_b128 v[190:193], v209 offset:50176
	ds_read_b128 v[178:181], v209 offset:51200
	ds_read_b128 v[182:185], v209 offset:52224
	ds_read_b128 v[170:173], v209 offset:53248
	ds_read_b128 v[174:177], v209 offset:54272
	ds_read_b128 v[162:165], v209 offset:55296
	ds_read_b128 v[166:169], v209 offset:56320
	global_load_lds_dwordx4 v[224:225], off
	v_lshl_add_u64 v[224:225], v[226:227], 0, s[42:43]
	s_add_i32 m0, s2, 0x2000
	v_lshl_add_u64 v[222:223], v[222:223], 0, s[44:45]
	s_add_i32 s2, s3, s33
	global_load_lds_dwordx4 v[224:225], off
	v_lshl_add_u64 v[224:225], v[222:223], 0, v[198:199]
	s_mov_b32 m0, s2
	v_lshl_add_u64 v[222:223], v[222:223], 0, v[200:201]
	global_load_lds_dwordx4 v[224:225], off
	s_add_i32 m0, s2, 0x2000
	v_lshl_add_u64 v[194:195], v[194:195], 0, s[42:43]
	global_load_lds_dwordx4 v[222:223], off
	s_mov_b32 m0, s76
	s_and_b64 vcc, exec, s[62:63]
	global_load_lds_dwordx4 v[194:195], off
	v_lshl_add_u64 v[194:195], v[196:197], 0, s[42:43]
	s_mov_b32 m0, s77
	s_nop 0
	global_load_lds_dwordx4 v[194:195], off
	s_waitcnt vmcnt(8)
	s_waitcnt lgkmcnt(0)
	s_barrier
	s_cbranch_vccnz .LBB0_1399
	s_setprio 1
	s_waitcnt lgkmcnt(0)
	v_mfma_f32_16x16x32_bf16 v[60:63], v[146:149], v[186:189], v[60:63]
	v_mfma_f32_16x16x32_bf16 v[56:59], v[154:157], v[186:189], v[56:59]
	v_mfma_f32_16x16x32_bf16 v[44:47], v[146:149], v[178:181], v[44:47]
	v_mfma_f32_16x16x32_bf16 v[40:43], v[154:157], v[178:181], v[40:43]
	v_mfma_f32_16x16x32_bf16 v[28:31], v[146:149], v[170:173], v[28:31]
	v_mfma_f32_16x16x32_bf16 v[24:27], v[154:157], v[170:173], v[24:27]
	v_mfma_f32_16x16x32_bf16 v[12:15], v[146:149], v[162:165], v[12:15]
	v_mfma_f32_16x16x32_bf16 v[8:11], v[154:157], v[162:165], v[8:11]
	v_mfma_f32_16x16x32_bf16 v[60:63], v[150:153], v[190:193], v[60:63]
	v_mfma_f32_16x16x32_bf16 v[56:59], v[158:161], v[190:193], v[56:59]
	v_mfma_f32_16x16x32_bf16 v[44:47], v[150:153], v[182:185], v[44:47]
	v_mfma_f32_16x16x32_bf16 v[40:43], v[158:161], v[182:185], v[40:43]
	v_mfma_f32_16x16x32_bf16 v[28:31], v[150:153], v[174:177], v[28:31]
	v_mfma_f32_16x16x32_bf16 v[24:27], v[158:161], v[174:177], v[24:27]
	v_mfma_f32_16x16x32_bf16 v[12:15], v[150:153], v[166:169], v[12:15]
	v_mfma_f32_16x16x32_bf16 v[8:11], v[158:161], v[166:169], v[8:11]
	v_mfma_f32_16x16x32_bf16 v[52:55], v[130:133], v[186:189], v[52:55]
	v_mfma_f32_16x16x32_bf16 v[48:51], v[138:141], v[186:189], v[48:51]
	v_mfma_f32_16x16x32_bf16 v[36:39], v[130:133], v[178:181], v[36:39]
	v_mfma_f32_16x16x32_bf16 v[32:35], v[138:141], v[178:181], v[32:35]
	v_mfma_f32_16x16x32_bf16 v[20:23], v[130:133], v[170:173], v[20:23]
	v_mfma_f32_16x16x32_bf16 v[16:19], v[138:141], v[170:173], v[16:19]
	v_mfma_f32_16x16x32_bf16 v[4:7], v[130:133], v[162:165], v[4:7]
	v_mfma_f32_16x16x32_bf16 v[0:3], v[138:141], v[162:165], v[0:3]
	v_mfma_f32_16x16x32_bf16 v[52:55], v[134:137], v[190:193], v[52:55]
	v_mfma_f32_16x16x32_bf16 v[48:51], v[142:145], v[190:193], v[48:51]
	v_mfma_f32_16x16x32_bf16 v[36:39], v[134:137], v[182:185], v[36:39]
	v_mfma_f32_16x16x32_bf16 v[32:35], v[142:145], v[182:185], v[32:35]
	v_mfma_f32_16x16x32_bf16 v[20:23], v[134:137], v[174:177], v[20:23]
	v_mfma_f32_16x16x32_bf16 v[16:19], v[142:145], v[174:177], v[16:19]
	v_mfma_f32_16x16x32_bf16 v[4:7], v[134:137], v[166:169], v[4:7]
	v_mfma_f32_16x16x32_bf16 v[0:3], v[142:145], v[166:169], v[0:3]
	s_setprio 0
	s_branch .LBB0_1399

.LBB0_1443:
	s_lshl_b32 s72, s19, 7
	s_add_u32 s29, s76, s72
	s_addc_u32 s30, s77, 0
	s_add_u32 s22, s29, 0x100
	s_addc_u32 s23, s30, 0
	v_lshl_add_u64 v[144:145], v[142:143], 0, s[72:73]
	s_and_b64 s[2:3], s[60:61], exec
	v_lshl_add_u64 v[144:145], v[144:145], 0, s[46:47]
	s_cselect_b32 s23, s67, s23
	s_cselect_b32 s22, s66, s22
	v_cndmask_b32_e64 v145, v145, v141, s[60:61]
	v_cndmask_b32_e64 v144, v144, v140, s[60:61]
	s_add_i32 s60, 0, 0x10000
	v_add_u32_e32 v128, s60, v147
	s_add_i32 s61, 0, 0x14000
	ds_read_b128 v[150:153], v128
	ds_read_b128 v[154:157], v128 offset:1024
	ds_read_b128 v[158:161], v128 offset:2048
	ds_read_b128 v[162:165], v128 offset:3072
	v_add_u32_e32 v128, s61, v147
	ds_read_b128 v[166:169], v128
	ds_read_b128 v[170:173], v128 offset:1024
	ds_read_b128 v[174:177], v128 offset:2048
	ds_read_b128 v[178:181], v128 offset:3072
	s_add_u32 s2, s29, 0x20080
	s_addc_u32 s3, s30, 0
	v_lshl_add_u64 v[194:195], s[2:3], 0, v[130:131]
	s_add_i32 m0, s35, 0xc000
	ds_read_b128 v[182:185], v148
	ds_read_b128 v[186:189], v148 offset:1024
	ds_read_b128 v[190:193], v148 offset:2048
	ds_read_b128 v[198:201], v148 offset:3072
	ds_read_b128 v[202:205], v148 offset:4096
	ds_read_b128 v[206:209], v148 offset:5120
	ds_read_b128 v[210:213], v148 offset:6144
	ds_read_b128 v[214:217], v148 offset:7168
	global_load_lds_dwordx4 v[194:195], off
	v_lshl_add_u64 v[194:195], s[2:3], 0, v[134:135]
	s_add_i32 m0, s35, 0xe000
	s_nop 0
	global_load_lds_dwordx4 v[194:195], off
	s_waitcnt vmcnt(8)
	s_waitcnt lgkmcnt(0)
	s_barrier
	s_setprio 1
	s_waitcnt lgkmcnt(0)
	v_mfma_f32_16x16x32_bf16 v[124:127], v[150:153], v[182:185], v[124:127]
	v_mfma_f32_16x16x32_bf16 v[120:123], v[158:161], v[182:185], v[120:123]
	v_mfma_f32_16x16x32_bf16 v[112:115], v[150:153], v[190:193], v[112:115]
	v_mfma_f32_16x16x32_bf16 v[104:107], v[158:161], v[190:193], v[104:107]
	v_mfma_f32_16x16x32_bf16 v[96:99], v[150:153], v[202:205], v[96:99]
	v_mfma_f32_16x16x32_bf16 v[88:91], v[158:161], v[202:205], v[88:91]
	v_mfma_f32_16x16x32_bf16 v[80:83], v[150:153], v[210:213], v[80:83]
	v_mfma_f32_16x16x32_bf16 v[72:75], v[158:161], v[210:213], v[72:75]
	v_mfma_f32_16x16x32_bf16 v[124:127], v[154:157], v[186:189], v[124:127]
	v_mfma_f32_16x16x32_bf16 v[120:123], v[162:165], v[186:189], v[120:123]
	v_mfma_f32_16x16x32_bf16 v[112:115], v[154:157], v[198:201], v[112:115]
	v_mfma_f32_16x16x32_bf16 v[104:107], v[162:165], v[198:201], v[104:107]
	v_mfma_f32_16x16x32_bf16 v[96:99], v[154:157], v[206:209], v[96:99]
	v_mfma_f32_16x16x32_bf16 v[88:91], v[162:165], v[206:209], v[88:91]
	v_mfma_f32_16x16x32_bf16 v[80:83], v[154:157], v[214:217], v[80:83]
	v_mfma_f32_16x16x32_bf16 v[72:75], v[162:165], v[214:217], v[72:75]
	v_mfma_f32_16x16x32_bf16 v[116:119], v[166:169], v[182:185], v[116:119]
	v_mfma_f32_16x16x32_bf16 v[108:111], v[174:177], v[182:185], v[108:111]
	v_mfma_f32_16x16x32_bf16 v[100:103], v[166:169], v[190:193], v[100:103]
	v_mfma_f32_16x16x32_bf16 v[92:95], v[174:177], v[190:193], v[92:95]
	v_mfma_f32_16x16x32_bf16 v[84:87], v[166:169], v[202:205], v[84:87]
	v_mfma_f32_16x16x32_bf16 v[76:79], v[174:177], v[202:205], v[76:79]
	v_mfma_f32_16x16x32_bf16 v[68:71], v[166:169], v[210:213], v[68:71]
	v_mfma_f32_16x16x32_bf16 v[64:67], v[174:177], v[210:213], v[64:67]
	v_mfma_f32_16x16x32_bf16 v[116:119], v[170:173], v[186:189], v[116:119]
	v_mfma_f32_16x16x32_bf16 v[108:111], v[178:181], v[186:189], v[108:111]
	v_mfma_f32_16x16x32_bf16 v[100:103], v[170:173], v[198:201], v[100:103]
	v_mfma_f32_16x16x32_bf16 v[92:95], v[178:181], v[198:201], v[92:95]
	v_mfma_f32_16x16x32_bf16 v[84:87], v[170:173], v[206:209], v[84:87]
	v_mfma_f32_16x16x32_bf16 v[76:79], v[178:181], v[206:209], v[76:79]
	v_mfma_f32_16x16x32_bf16 v[68:71], v[170:173], v[214:217], v[68:71]
	v_mfma_f32_16x16x32_bf16 v[64:67], v[178:181], v[214:217], v[64:67]
	s_setprio 0
	s_barrier
	s_add_i32 s2, s60, s33
	v_lshl_add_u64 v[194:195], v[144:145], 0, v[132:133]
	s_mov_b32 m0, s2
	ds_read_b128 v[182:185], v148 offset:16384
	ds_read_b128 v[186:189], v148 offset:17408
	ds_read_b128 v[190:193], v148 offset:18432
	ds_read_b128 v[198:201], v148 offset:19456
	ds_read_b128 v[202:205], v148 offset:20480
	ds_read_b128 v[206:209], v148 offset:21504
	ds_read_b128 v[210:213], v148 offset:22528
	ds_read_b128 v[214:217], v148 offset:23552
	global_load_lds_dwordx4 v[194:195], off
	v_lshl_add_u64 v[196:197], v[144:145], 0, v[136:137]
	s_add_i32 m0, s2, 0x2000
	v_lshl_add_u64 v[218:219], v[144:145], 0, s[48:49]
	s_add_i32 s2, s61, s33
	global_load_lds_dwordx4 v[196:197], off
	v_lshl_add_u64 v[220:221], v[218:219], 0, v[132:133]
	s_mov_b32 m0, s2
	v_lshl_add_u64 v[218:219], v[218:219], 0, v[136:137]
	global_load_lds_dwordx4 v[220:221], off
	s_add_i32 m0, s2, 0x2000
	v_lshl_add_u64 v[220:221], s[22:23], 0, v[134:135]
	global_load_lds_dwordx4 v[218:219], off
	v_lshl_add_u64 v[218:219], s[22:23], 0, v[130:131]
	s_mov_b32 m0, s35
	s_nop 0
	global_load_lds_dwordx4 v[218:219], off
	s_mov_b32 m0, s36
	s_nop 0
	global_load_lds_dwordx4 v[220:221], off
	s_waitcnt vmcnt(8)
	s_waitcnt lgkmcnt(0)
	s_barrier
	s_setprio 1
	s_waitcnt lgkmcnt(0)
	v_mfma_f32_16x16x32_bf16 v[60:63], v[150:153], v[182:185], v[60:63]
	v_mfma_f32_16x16x32_bf16 v[56:59], v[158:161], v[182:185], v[56:59]
	v_mfma_f32_16x16x32_bf16 v[48:51], v[150:153], v[190:193], v[48:51]
	v_mfma_f32_16x16x32_bf16 v[40:43], v[158:161], v[190:193], v[40:43]
	v_mfma_f32_16x16x32_bf16 v[32:35], v[150:153], v[202:205], v[32:35]
	v_mfma_f32_16x16x32_bf16 v[24:27], v[158:161], v[202:205], v[24:27]
	v_mfma_f32_16x16x32_bf16 v[16:19], v[150:153], v[210:213], v[16:19]
	v_mfma_f32_16x16x32_bf16 v[8:11], v[158:161], v[210:213], v[8:11]
	v_mfma_f32_16x16x32_bf16 v[60:63], v[154:157], v[186:189], v[60:63]
	v_mfma_f32_16x16x32_bf16 v[56:59], v[162:165], v[186:189], v[56:59]
	v_mfma_f32_16x16x32_bf16 v[48:51], v[154:157], v[198:201], v[48:51]
	v_mfma_f32_16x16x32_bf16 v[40:43], v[162:165], v[198:201], v[40:43]
	v_mfma_f32_16x16x32_bf16 v[32:35], v[154:157], v[206:209], v[32:35]
	v_mfma_f32_16x16x32_bf16 v[24:27], v[162:165], v[206:209], v[24:27]
	v_mfma_f32_16x16x32_bf16 v[16:19], v[154:157], v[214:217], v[16:19]
	v_mfma_f32_16x16x32_bf16 v[8:11], v[162:165], v[214:217], v[8:11]
	v_mfma_f32_16x16x32_bf16 v[52:55], v[166:169], v[182:185], v[52:55]
	v_mfma_f32_16x16x32_bf16 v[44:47], v[174:177], v[182:185], v[44:47]
	v_mfma_f32_16x16x32_bf16 v[36:39], v[166:169], v[190:193], v[36:39]
	v_mfma_f32_16x16x32_bf16 v[28:31], v[174:177], v[190:193], v[28:31]
	v_mfma_f32_16x16x32_bf16 v[20:23], v[166:169], v[202:205], v[20:23]
	v_mfma_f32_16x16x32_bf16 v[12:15], v[174:177], v[202:205], v[12:15]
	v_mfma_f32_16x16x32_bf16 v[4:7], v[166:169], v[210:213], v[4:7]
	v_mfma_f32_16x16x32_bf16 v[0:3], v[174:177], v[210:213], v[0:3]
	v_mfma_f32_16x16x32_bf16 v[52:55], v[170:173], v[186:189], v[52:55]
	v_mfma_f32_16x16x32_bf16 v[44:47], v[178:181], v[186:189], v[44:47]
	v_mfma_f32_16x16x32_bf16 v[36:39], v[170:173], v[198:201], v[36:39]
	v_mfma_f32_16x16x32_bf16 v[28:31], v[178:181], v[198:201], v[28:31]
	v_mfma_f32_16x16x32_bf16 v[20:23], v[170:173], v[206:209], v[20:23]
	v_mfma_f32_16x16x32_bf16 v[12:15], v[178:181], v[206:209], v[12:15]
	v_mfma_f32_16x16x32_bf16 v[4:7], v[170:173], v[214:217], v[4:7]
	v_mfma_f32_16x16x32_bf16 v[0:3], v[178:181], v[214:217], v[0:3]
	s_setprio 0
	s_barrier
	s_add_i32 s29, 0, 0x18000
	v_add_u32_e32 v128, s29, v147
	s_add_i32 s30, 0, 0x1c000
	ds_read_b128 v[150:153], v128
	ds_read_b128 v[154:157], v128 offset:1024
	ds_read_b128 v[158:161], v128 offset:2048
	ds_read_b128 v[162:165], v128 offset:3072
	v_add_u32_e32 v128, s30, v147
	ds_read_b128 v[166:169], v128
	ds_read_b128 v[170:173], v128 offset:1024
	ds_read_b128 v[174:177], v128 offset:2048
	ds_read_b128 v[178:181], v128 offset:3072
	s_add_u32 s2, s22, 0x20000
	s_addc_u32 s3, s23, 0
	s_mov_b32 m0, s37
	v_lshl_add_u64 v[222:223], s[2:3], 0, v[130:131]
	ds_read_b128 v[182:185], v148 offset:32768
	ds_read_b128 v[186:189], v148 offset:33792
	ds_read_b128 v[190:193], v148 offset:34816
	ds_read_b128 v[198:201], v148 offset:35840
	ds_read_b128 v[202:205], v148 offset:36864
	ds_read_b128 v[206:209], v148 offset:37888
	ds_read_b128 v[210:213], v148 offset:38912
	ds_read_b128 v[214:217], v148 offset:39936
	global_load_lds_dwordx4 v[222:223], off
	v_lshl_add_u64 v[222:223], s[2:3], 0, v[134:135]
	s_mov_b32 m0, s38
	s_nop 0
	global_load_lds_dwordx4 v[222:223], off
	s_waitcnt vmcnt(8)
	s_waitcnt lgkmcnt(0)
	s_barrier
	s_setprio 1
	s_waitcnt lgkmcnt(0)
	v_mfma_f32_16x16x32_bf16 v[124:127], v[150:153], v[182:185], v[124:127]
	v_mfma_f32_16x16x32_bf16 v[120:123], v[158:161], v[182:185], v[120:123]
	v_mfma_f32_16x16x32_bf16 v[112:115], v[150:153], v[190:193], v[112:115]
	v_mfma_f32_16x16x32_bf16 v[104:107], v[158:161], v[190:193], v[104:107]
	v_mfma_f32_16x16x32_bf16 v[96:99], v[150:153], v[202:205], v[96:99]
	v_mfma_f32_16x16x32_bf16 v[88:91], v[158:161], v[202:205], v[88:91]
	v_mfma_f32_16x16x32_bf16 v[80:83], v[150:153], v[210:213], v[80:83]
	v_mfma_f32_16x16x32_bf16 v[72:75], v[158:161], v[210:213], v[72:75]
	v_mfma_f32_16x16x32_bf16 v[124:127], v[154:157], v[186:189], v[124:127]
	v_mfma_f32_16x16x32_bf16 v[120:123], v[162:165], v[186:189], v[120:123]
	v_mfma_f32_16x16x32_bf16 v[112:115], v[154:157], v[198:201], v[112:115]
	v_mfma_f32_16x16x32_bf16 v[104:107], v[162:165], v[198:201], v[104:107]
	v_mfma_f32_16x16x32_bf16 v[96:99], v[154:157], v[206:209], v[96:99]
	v_mfma_f32_16x16x32_bf16 v[88:91], v[162:165], v[206:209], v[88:91]
	v_mfma_f32_16x16x32_bf16 v[80:83], v[154:157], v[214:217], v[80:83]
	v_mfma_f32_16x16x32_bf16 v[72:75], v[162:165], v[214:217], v[72:75]
	v_mfma_f32_16x16x32_bf16 v[116:119], v[166:169], v[182:185], v[116:119]
	v_mfma_f32_16x16x32_bf16 v[108:111], v[174:177], v[182:185], v[108:111]
	v_mfma_f32_16x16x32_bf16 v[100:103], v[166:169], v[190:193], v[100:103]
	v_mfma_f32_16x16x32_bf16 v[92:95], v[174:177], v[190:193], v[92:95]
	v_mfma_f32_16x16x32_bf16 v[84:87], v[166:169], v[202:205], v[84:87]
	v_mfma_f32_16x16x32_bf16 v[76:79], v[174:177], v[202:205], v[76:79]
	v_mfma_f32_16x16x32_bf16 v[68:71], v[166:169], v[210:213], v[68:71]
	v_mfma_f32_16x16x32_bf16 v[64:67], v[174:177], v[210:213], v[64:67]
	v_mfma_f32_16x16x32_bf16 v[116:119], v[170:173], v[186:189], v[116:119]
	v_mfma_f32_16x16x32_bf16 v[108:111], v[178:181], v[186:189], v[108:111]
	v_mfma_f32_16x16x32_bf16 v[100:103], v[170:173], v[198:201], v[100:103]
	v_mfma_f32_16x16x32_bf16 v[92:95], v[178:181], v[198:201], v[92:95]
	v_mfma_f32_16x16x32_bf16 v[84:87], v[170:173], v[206:209], v[84:87]
	v_mfma_f32_16x16x32_bf16 v[76:79], v[178:181], v[206:209], v[76:79]
	v_mfma_f32_16x16x32_bf16 v[68:71], v[170:173], v[214:217], v[68:71]
	v_mfma_f32_16x16x32_bf16 v[64:67], v[178:181], v[214:217], v[64:67]
	s_setprio 0
	s_barrier
	s_add_i32 s2, s29, s33
	v_lshl_add_u64 v[194:195], v[194:195], 0, s[42:43]
	s_mov_b32 m0, s2
	ds_read_b128 v[182:185], v148 offset:49152
	ds_read_b128 v[186:189], v148 offset:50176
	ds_read_b128 v[190:193], v148 offset:51200
	ds_read_b128 v[198:201], v148 offset:52224
	ds_read_b128 v[202:205], v148 offset:53248
	ds_read_b128 v[206:209], v148 offset:54272
	ds_read_b128 v[210:213], v148 offset:55296
	ds_read_b128 v[214:217], v148 offset:56320
	global_load_lds_dwordx4 v[194:195], off
	v_lshl_add_u64 v[194:195], v[196:197], 0, s[42:43]
	s_add_i32 m0, s2, 0x2000
	v_lshl_add_u64 v[144:145], v[144:145], 0, s[50:51]
	s_add_i32 s2, s30, s33
	global_load_lds_dwordx4 v[194:195], off
	v_lshl_add_u64 v[194:195], v[144:145], 0, v[132:133]
	s_mov_b32 m0, s2
	v_lshl_add_u64 v[144:145], v[144:145], 0, v[136:137]
	global_load_lds_dwordx4 v[194:195], off
	s_add_i32 m0, s2, 0x2000
	s_nop 0
	global_load_lds_dwordx4 v[144:145], off
	v_lshl_add_u64 v[144:145], v[218:219], 0, s[42:43]
	s_mov_b32 m0, s39
	s_nop 0
	global_load_lds_dwordx4 v[144:145], off
	v_lshl_add_u64 v[144:145], v[220:221], 0, s[42:43]
	s_mov_b32 m0, s53
	s_nop 0
	global_load_lds_dwordx4 v[144:145], off
	s_waitcnt vmcnt(8)
	s_waitcnt lgkmcnt(0)
	s_barrier
	s_setprio 1
	s_waitcnt lgkmcnt(0)
	v_mfma_f32_16x16x32_bf16 v[60:63], v[150:153], v[182:185], v[60:63]
	v_mfma_f32_16x16x32_bf16 v[56:59], v[158:161], v[182:185], v[56:59]
	v_mfma_f32_16x16x32_bf16 v[48:51], v[150:153], v[190:193], v[48:51]
	v_mfma_f32_16x16x32_bf16 v[40:43], v[158:161], v[190:193], v[40:43]
	v_mfma_f32_16x16x32_bf16 v[32:35], v[150:153], v[202:205], v[32:35]
	v_mfma_f32_16x16x32_bf16 v[24:27], v[158:161], v[202:205], v[24:27]
	v_mfma_f32_16x16x32_bf16 v[16:19], v[150:153], v[210:213], v[16:19]
	v_mfma_f32_16x16x32_bf16 v[8:11], v[158:161], v[210:213], v[8:11]
	v_mfma_f32_16x16x32_bf16 v[60:63], v[154:157], v[186:189], v[60:63]
	v_mfma_f32_16x16x32_bf16 v[56:59], v[162:165], v[186:189], v[56:59]
	v_mfma_f32_16x16x32_bf16 v[48:51], v[154:157], v[198:201], v[48:51]
	v_mfma_f32_16x16x32_bf16 v[40:43], v[162:165], v[198:201], v[40:43]
	v_mfma_f32_16x16x32_bf16 v[32:35], v[154:157], v[206:209], v[32:35]
	v_mfma_f32_16x16x32_bf16 v[24:27], v[162:165], v[206:209], v[24:27]
	v_mfma_f32_16x16x32_bf16 v[16:19], v[154:157], v[214:217], v[16:19]
	v_mfma_f32_16x16x32_bf16 v[8:11], v[162:165], v[214:217], v[8:11]
	v_mfma_f32_16x16x32_bf16 v[52:55], v[166:169], v[182:185], v[52:55]
	v_mfma_f32_16x16x32_bf16 v[44:47], v[174:177], v[182:185], v[44:47]
	v_mfma_f32_16x16x32_bf16 v[36:39], v[166:169], v[190:193], v[36:39]
	v_mfma_f32_16x16x32_bf16 v[28:31], v[174:177], v[190:193], v[28:31]
	v_mfma_f32_16x16x32_bf16 v[20:23], v[166:169], v[202:205], v[20:23]
	v_mfma_f32_16x16x32_bf16 v[12:15], v[174:177], v[202:205], v[12:15]
	v_mfma_f32_16x16x32_bf16 v[4:7], v[166:169], v[210:213], v[4:7]
	v_mfma_f32_16x16x32_bf16 v[0:3], v[174:177], v[210:213], v[0:3]
	v_mfma_f32_16x16x32_bf16 v[52:55], v[170:173], v[186:189], v[52:55]
	v_mfma_f32_16x16x32_bf16 v[44:47], v[178:181], v[186:189], v[44:47]
	v_mfma_f32_16x16x32_bf16 v[36:39], v[170:173], v[198:201], v[36:39]
	v_mfma_f32_16x16x32_bf16 v[28:31], v[178:181], v[198:201], v[28:31]
	v_mfma_f32_16x16x32_bf16 v[20:23], v[170:173], v[206:209], v[20:23]
	v_mfma_f32_16x16x32_bf16 v[12:15], v[178:181], v[206:209], v[12:15]
	v_mfma_f32_16x16x32_bf16 v[4:7], v[170:173], v[214:217], v[4:7]
	v_mfma_f32_16x16x32_bf16 v[0:3], v[178:181], v[214:217], v[0:3]
	s_setprio 0
	s_barrier
	s_add_i32 s2, s19, 2
	s_cmp_gt_u32 s19, 5
	s_mov_b32 s19, s2
	s_cbranch_scc1 .LBB0_1450
